# adds: dead m0 save/restore pairs around the asm LDS-DMA statements removed (attention, retention scan/main)
# baseline (speedup 1.0000x reference)
; __device__ __forceinline__ void glds16(const void* gsrc, unsigned lds_dst) { unsigned keep;
;     asm volatile("s_mov_b32 %0, m0\n\ts_mov_b32 m0, %2\n\ts_nop 0\n\tglobal_load_lds_dwordx4 %1, off\n\ts_mov_b32 m0, %0" : "=&s"(keep) : "v"(gsrc), "s"(lds_dst) : "memory"); }
; __device__ __forceinline__ void ret_scan_phase(Frame& F, const bf16* PROJ, bf16* ST, const float (&lg2)[4]) { LTID();
;     ...
;         int tid = tid_; asm volatile("" : "+v"(tid));
;         const int lane = tid & 63, r32 = lane & 31, hh = lane >> 5, wid = __builtin_amdgcn_readfirstlane(tid >> 6);
;         const int voff = (4 * hh + ((lane & 15) >> 2)) * 64 + ((lane >> 4) & 1) * 32 + (lane & 3) * 8;
;         const int bh = L >> 4, dkh = (L >> 3) & 1, e8 = L & 7, h = bh & 3;
;         const float lgh = h == 0 ? lg2[0] : h == 1 ? lg2[1] : h == 2 ? lg2[2] : lg2[3];
;         const float gC = __builtin_amdgcn_exp2f(128.f * lgh);
;         const int trow = lane >> 2, chl = lane & 3;
;         const bf16* ksrc0 = PROJ + (size_t)T * 1024 + ((size_t)bh * SEQ + 16 * ((2 * wid) & 3) + trow) * 256 + dkh * 128 + ((2 * wid) >> 2) * 32 + chl * 8;
;         const bf16* ksrc1 = PROJ + (size_t)T * 1024 + ((size_t)bh * SEQ + 16 * ((2 * wid + 1) & 3) + trow) * 256 + dkh * 128 + ((2 * wid + 1) >> 2) * 32 + chl * 8;
;         const bf16* vsrc = PROJ + (size_t)2 * T * 1024 + ((size_t)bh * SEQ + 16 * (wid & 3) + trow) * 512 + e8 * 64 + (wid >> 2) * 32 + chl * 8;
;         const unsigned ldsb = (unsigned)(uintptr_t)lds;
;     ...
;         f32x16 st = (f32x16){0.f, 0.f, 0.f, 0.f, 0.f, 0.f, 0.f, 0.f, 0.f, 0.f, 0.f, 0.f, 0.f, 0.f, 0.f, 0.f};
;         const int el = (wid >> 2) * 32 + r32;
;         bf16* stg = ST + ((size_t)bh * 64 * 512 + e8 * 64) * 256 + dkh * 128;
;         RS_DMA(0, 0); RS_DMA(1, 1); RS_DMA(2, 2);
.LBB0_291:
	s_ashr_i32 s22, s18, 6
	s_ashr_i32 s7, s6, 31
	v_lshlrev_b32_e32 v27, 4, v2
	v_lshlrev_b32_e32 v5, 3, v2
	s_lshl_b64 s[12:13], s[6:7], 13
	s_lshl_b32 s20, s22, 5
	v_bfe_u32 v3, v2, 5, 1
	v_and_b32_e32 v0, 0xc0, v27
	v_lshlrev_b32_e32 v4, 1, v2
	v_and_b32_e32 v8, 24, v5
	v_exp_f32_e32 v18, s19
	s_lshl_b32 s19, s22, 1
	s_and_b32 s20, s20, 32
	v_mov_b32_e32 v5, s13
	s_lshl_b32 s13, s2, 5
	v_lshl_or_b32 v0, v3, 8, v0
	v_and_b32_e32 v4, 32, v4
	v_bfe_u32 v10, v2, 2, 4
	s_or_b32 s20, s12, s20
	s_and_b32 s78, s13, 0x100
	s_ashr_i32 s13, s18, 2
	s_or_b32 s19, s19, 1
	v_or3_b32 v40, v0, v4, v8
	v_or_b32_e32 v4, s20, v10
	s_and_b32 s20, s13, 0xffffffe0
	s_lshl_b32 s13, s19, 4
	s_and_b32 s13, s13, 48
	s_or_b32 s13, s12, s13
	v_lshlrev_b64 v[6:7], 9, v[4:5]
	v_or_b32_e32 v4, s13, v10
	v_lshlrev_b32_e32 v0, 1, v8
	v_lshlrev_b64 v[8:9], 9, v[4:5]
	v_lshl_add_u64 v[6:7], s[8:9], 0, v[6:7]
	s_ashr_i32 s21, s20, 31
	v_lshl_add_u64 v[8:9], s[8:9], 0, v[8:9]
	v_lshl_add_u64 v[6:7], v[6:7], 0, s[78:79]
	s_lshl_b64 s[20:21], s[20:21], 1
	v_lshl_add_u64 v[8:9], v[8:9], 0, s[78:79]
	v_lshl_add_u64 v[6:7], v[6:7], 0, s[20:21]
	v_lshl_add_u64 v[8:9], v[8:9], 0, s[20:21]
	s_and_b32 s21, s22, 3
	s_lshl_b32 s13, s21, 4
	s_or_b32 s12, s12, s13
	v_or_b32_e32 v4, s12, v10
	s_lshl_b32 s12, s2, 6
	v_lshlrev_b64 v[4:5], 10, v[4:5]
	s_and_b32 s20, s12, 0x1c0
	v_lshl_add_u64 v[4:5], s[10:11], 0, v[4:5]
	s_lshl_b32 s12, s20, 1
	s_mov_b32 s13, s79
	s_ashr_i32 s23, s18, 8
	v_lshl_add_u64 v[4:5], v[4:5], 0, s[12:13]
	s_lshl_b32 s12, s23, 5
	s_ashr_i32 s13, s12, 31
	s_lshl_b64 s[6:7], s[6:7], 24
	v_lshl_add_u64 v[4:5], s[12:13], 1, v[4:5]
	s_add_u32 s6, s0, s6
	v_lshl_add_u64 v[6:7], v[6:7], 0, v[0:1]
	v_lshl_add_u64 v[8:9], v[8:9], 0, v[0:1]
	v_lshl_add_u64 v[4:5], v[4:5], 0, v[0:1]
	v_and_or_b32 v0, v2, 31, s12
	s_addc_u32 s7, s14, s7
	s_lshl_b32 s12, s20, 9
	s_add_u32 s6, s6, s12
	s_addc_u32 s7, s7, 0
	s_add_u32 s12, s6, s78
	s_addc_u32 s13, s7, 0
	s_lshl_b32 s18, s22, 11
	s_add_i32 s6, s18, 0
	s_lshl_b32 s19, s19, 10
	s_mov_b32 m0, s6
	s_nop 0
	global_load_lds_dwordx4 v[6:7], off
	s_add_i32 s6, s19, 0
	s_lshl_b32 s20, s22, 10
	s_mov_b32 m0, s6
	s_nop 0
	global_load_lds_dwordx4 v[8:9], off
	s_add_i32 s6, s20, 0
	s_add_i32 s7, s6, 0x4000
	s_mov_b32 m0, s7
	s_nop 0
	global_load_lds_dwordx4 v[4:5], off
	s_add_i32 s7, 0, 0x6000
	v_lshl_add_u64 v[10:11], v[6:7], 0, s[48:49]
	s_add_i32 s22, s18, s7
	s_mov_b32 m0, s22
	s_nop 0
	global_load_lds_dwordx4 v[10:11], off
	s_add_i32 s7, s19, s7
	v_lshl_add_u64 v[10:11], v[8:9], 0, s[48:49]
	s_mov_b32 m0, s7
	s_nop 0
	global_load_lds_dwordx4 v[10:11], off
	s_add_i32 s7, s6, 0xa000
	v_lshl_add_u64 v[10:11], v[4:5], 0, s[80:81]
	s_mov_b32 m0, s7
	s_nop 0
	global_load_lds_dwordx4 v[10:11], off
	s_add_i32 s7, 0, 0xc000
	v_lshl_add_u64 v[10:11], v[6:7], 0, s[80:81]
	s_add_i32 s22, s18, s7
	s_mov_b32 m0, s22
	s_nop 0
	global_load_lds_dwordx4 v[10:11], off
	v_lshl_add_u64 v[10:11], v[8:9], 0, s[80:81]
	s_add_i32 s7, s19, s7
	s_mov_b32 m0, s7
	s_nop 0
	global_load_lds_dwordx4 v[10:11], off
	s_add_i32 s6, s6, 0x10000
	v_lshl_add_u64 v[10:11], v[4:5], 0, s[76:77]
	s_mov_b32 m0, s6
	s_nop 0
	global_load_lds_dwordx4 v[10:11], off
	v_lshlrev_b32_e32 v0, 8, v0
	s_add_i32 s6, 0, 0x18000
	v_lshlrev_b32_e32 v3, 3, v3
	v_ashrrev_i32_e32 v24, 4, v2
	v_add3_u32 v42, s6, v0, v3
	v_xor_b32_e32 v0, v24, v2
	v_lshlrev_b32_e32 v0, 3, v0
	v_and_b32_e32 v26, 0x78, v0
	v_add_u32_e32 v0, 0x200, v2
	v_ashrrev_i32_e32 v20, 4, v0
	v_xor_b32_e32 v3, v20, v2
	s_lshl_b32 s7, s21, 2
	v_lshlrev_b32_e32 v41, 4, v0
	v_lshlrev_b32_e32 v0, 3, v3
	v_and_b32_e32 v10, 15, v2
	v_and_b32_e32 v22, 0x78, v0
	v_bitop3_b32 v0, s7, v2, 15 bitop3:0x78
	v_lshlrev_b32_e32 v43, 4, v0
	v_bitop3_b32 v0, s7, v10, 1 bitop3:0x36
	v_lshlrev_b32_e32 v44, 4, v0
	v_bitop3_b32 v0, s7, v10, 2 bitop3:0x36
	v_lshlrev_b32_e32 v45, 4, v0
	v_bitop3_b32 v0, s7, v10, 3 bitop3:0x36
	s_mov_b64 s[6:7], 0x30000
	v_ashrrev_i32_e32 v25, 31, v24
	v_ashrrev_i32_e32 v21, 31, v20
	v_lshl_add_u64 v[34:35], v[4:5], 0, s[6:7]
	s_mov_b64 s[6:7], 0x18000
	v_mov_b32_e32 v2, 0
	s_mov_b32 s15, 3
	s_addk_i32 s20, 0x4000
	s_lshl_b32 s21, s21, 12
	s_lshl_b32 s22, s23, 12
	v_lshlrev_b64 v[28:29], 9, v[24:25]
	v_lshlrev_b64 v[30:31], 9, v[20:21]
	v_lshlrev_b32_e32 v46, 4, v0
	v_mov_b32_e32 v32, v18
	v_mov_b32_e32 v33, v18
	v_lshl_add_u64 v[36:37], v[8:9], 0, s[6:7]
	v_lshl_add_u64 v[38:39], v[6:7], 0, s[6:7]
	v_mov_b32_e32 v3, v2
	v_mov_b32_e32 v4, v2
	v_mov_b32_e32 v5, v2
	v_mov_b32_e32 v6, v2
	v_mov_b32_e32 v7, v2
	v_mov_b32_e32 v8, v2
	v_mov_b32_e32 v9, v2
	v_mov_b32_e32 v10, v2
	v_mov_b32_e32 v11, v2
	v_mov_b32_e32 v12, v2
	v_mov_b32_e32 v13, v2
	v_mov_b32_e32 v14, v2
	v_mov_b32_e32 v15, v2
	v_mov_b32_e32 v16, v2
	v_mov_b32_e32 v17, v2
	s_branch .LBB0_294

; __device__ __forceinline__ void ret_scan_phase(Frame& F, const bf16* PROJ, bf16* ST, const float (&lg2)[4]) { LTID();
;     ...
;         for (int m = 0; m < 128; ++m) {
;             const int slot = m & 3, n = m >> 1;
;             if (m >= 3 && m + 2 < 128) asm volatile("s_waitcnt vmcnt(8) lgkmcnt(0)\n\ts_barrier" ::: "memory");
;             else if (m + 2 < 128) asm volatile("s_waitcnt vmcnt(6) lgkmcnt(0)\n\ts_barrier" ::: "memory");
;             else if (m + 1 < 128) asm volatile("s_waitcnt vmcnt(3) lgkmcnt(0)\n\ts_barrier" ::: "memory");
;             else asm volatile("s_waitcnt vmcnt(0) lgkmcnt(0)\n\ts_barrier" ::: "memory");
;             if (m + 3 < 128) RS_DMA(m + 3, (m + 3) & 3);
.LBB0_305:
	s_and_b32 s6, s15, 3
	s_mulk_i32 s6, 0x6000
	s_add_i32 s6, s6, 0
	s_add_i32 s7, s6, s18
	s_mov_b32 m0, s7
	s_nop 0
	global_load_lds_dwordx4 v[38:39], off
	s_add_i32 s7, s6, s19
	s_mov_b32 m0, s7
	s_nop 0
	global_load_lds_dwordx4 v[36:37], off
	s_add_i32 s6, s20, s6
	s_mov_b32 m0, s6
	s_nop 0
	global_load_lds_dwordx4 v[34:35], off

; #define GAS __attribute__((address_space(1)))
; #define RM_WAITBAR() asm volatile("s_waitcnt vmcnt(0) lgkmcnt(0)\n\ts_barrier" ::: "memory")
; #define RM_DMA_KS(buf) do { _Pragma("unroll") for (int i = 0; i < 8; ++i) { const int idx = tid + 512 * i, tok = idx >> 5, c = (idx & 31) ^ (tok & 31); \
;         glds16(PROJ + (size_t)T * 1024 + (hb0 + tok) * 256 + c * 8, (unsigned)__builtin_amdgcn_readfirstlane(ldsb + (buf) * 65536 + i * 8192)); } } while (0)
; __device__ __forceinline__ void ret_main_phase(Frame& F, const bf16* PROJ, const bf16* ST, bf16* AO) { LTID();
;     ...
;         int tid = tid_; asm volatile("" : "+v"(tid));
;         const int lane = tid & 63, r32 = lane & 31, hh = lane >> 5, wid = __builtin_amdgcn_readfirstlane(tid >> 6), rg = wid & 3, e2 = wid >> 2;
;         const int voff = (4 * hh + ((lane & 15) >> 2)) * 64 + ((lane >> 4) & 1) * 32 + (lane & 3) * 8;
;         const int U = L + uu, bh = U >> 6, n = U & 63, b = bh >> 2, h = bh & 3;
;         const size_t tokbase = (size_t)b * SEQ + (size_t)n * 128, hb0 = (size_t)bh * SEQ + (size_t)n * 128;
;         const bf16* qrow = PROJ + (hb0 + rg * 32 + r32) * 256 + 8 * hh;
;         const bf16* stb = ST + ((size_t)bh * 64 + n) * 512 * 256;
;         const unsigned ldsb = (unsigned)(uintptr_t)lds + wid * 1024;
;     ...
;         RM_DMA_KS(0);
;         bf16x8 pa[4][2];
;         {
;             bf16x8 qf[16];
; #pragma unroll
;             for (int s = 0; s < 16; ++s) qf[s] = *(const GAS bf16x8*)(qrow + 16 * s);
;             RM_WAITBAR();
;             asm volatile("" :: "v"(qf[0]), "v"(qf[1]), "v"(qf[2]), "v"(qf[3]), "v"(qf[4]), "v"(qf[5]), "v"(qf[6]), "v"(qf[7]), "v"(qf[8]), "v"(qf[9]), "v"(qf[10]), "v"(qf[11]), "v"(qf[12]), "v"(qf[13]), "v"(qf[14]), "v"(qf[15]));
.LBB0_365:
	v_mov_b32_e32 v210, v202
	s_nop 0
	v_readfirstlane_b32 s61, v210
	s_ashr_i32 s0, s61, 6
	s_and_b32 s66, s0, 3
	s_lshl_b32 s64, s66, 5
	v_and_b32_e32 v213, 31, v210
	s_add_u32 s34, s24, s30
	s_waitcnt vmcnt(0)
	v_ashrrev_i32_e32 v4, 5, v210
	v_or_b32_e32 v0, s64, v213
	s_addc_u32 s35, s25, s31
	v_ashrrev_i32_e32 v5, 31, v4
	v_lshl_add_u64 v[2:3], s[34:35], 0, v[0:1]
	v_xor_b32_e32 v0, v4, v210
	v_lshl_add_u64 v[4:5], s[34:35], 0, v[4:5]
	v_lshlrev_b64 v[4:5], 9, v[4:5]
	v_lshlrev_b32_e32 v0, 4, v0
	v_lshl_add_u64 v[4:5], s[14:15], 0, v[4:5]
	v_and_b32_e32 v0, 0x1f0, v0
	s_lshl_b32 s0, s0, 10
	v_lshl_add_u64 v[4:5], v[4:5], 0, v[0:1]
	v_add_u32_e32 v209, 0x200, v210
	s_add_i32 s65, s0, 0
	s_mov_b32 m0, s65
	s_nop 0
	global_load_lds_dwordx4 v[4:5], off
	v_ashrrev_i32_e32 v4, 5, v209
	v_ashrrev_i32_e32 v5, 31, v4
	v_xor_b32_e32 v0, v4, v210
	v_lshl_add_u64 v[4:5], s[34:35], 0, v[4:5]
	v_lshlrev_b64 v[4:5], 9, v[4:5]
	v_lshlrev_b32_e32 v0, 4, v0
	v_lshl_add_u64 v[4:5], s[14:15], 0, v[4:5]
	v_and_b32_e32 v0, 0x1f0, v0
	v_lshl_add_u64 v[4:5], v[4:5], 0, v[0:1]
	v_add_u32_e32 v208, 0x400, v210
	s_add_i32 s68, s65, 0x2000
	s_mov_b32 m0, s68
	s_nop 0
	global_load_lds_dwordx4 v[4:5], off
	v_ashrrev_i32_e32 v4, 5, v208
	v_ashrrev_i32_e32 v5, 31, v4
	v_xor_b32_e32 v0, v4, v210
	v_lshl_add_u64 v[4:5], s[34:35], 0, v[4:5]
	v_lshlrev_b64 v[4:5], 9, v[4:5]
	v_lshlrev_b32_e32 v0, 4, v0
	v_lshl_add_u64 v[4:5], s[14:15], 0, v[4:5]
	v_and_b32_e32 v0, 0x1f0, v0
	v_lshl_add_u64 v[4:5], v[4:5], 0, v[0:1]
	v_add_u32_e32 v207, 0x600, v210
	s_add_i32 s69, s65, 0x4000
	s_mov_b32 m0, s69
	s_nop 0
	global_load_lds_dwordx4 v[4:5], off
	v_ashrrev_i32_e32 v4, 5, v207
	v_ashrrev_i32_e32 v5, 31, v4
	v_xor_b32_e32 v0, v4, v210
	v_lshl_add_u64 v[4:5], s[34:35], 0, v[4:5]
	v_lshlrev_b64 v[4:5], 9, v[4:5]
	v_lshlrev_b32_e32 v0, 4, v0
	v_lshl_add_u64 v[4:5], s[14:15], 0, v[4:5]
	v_and_b32_e32 v0, 0x1f0, v0
	v_lshl_add_u64 v[4:5], v[4:5], 0, v[0:1]
	v_add_u32_e32 v206, 0x800, v210
	s_add_i32 s70, s65, 0x6000
	s_mov_b32 m0, s70
	s_nop 0
	global_load_lds_dwordx4 v[4:5], off
	v_ashrrev_i32_e32 v4, 5, v206
	v_ashrrev_i32_e32 v5, 31, v4
	v_xor_b32_e32 v0, v4, v210
	v_lshl_add_u64 v[4:5], s[34:35], 0, v[4:5]
	v_lshlrev_b64 v[4:5], 9, v[4:5]
	v_lshlrev_b32_e32 v0, 4, v0
	v_lshl_add_u64 v[4:5], s[14:15], 0, v[4:5]
	v_and_b32_e32 v0, 0x1f0, v0
	v_lshl_add_u64 v[4:5], v[4:5], 0, v[0:1]
	v_add_u32_e32 v205, 0xa00, v210
	s_add_i32 s46, s65, 0x8000
	s_mov_b32 m0, s46
	s_nop 0
	global_load_lds_dwordx4 v[4:5], off
	v_ashrrev_i32_e32 v4, 5, v205
	v_ashrrev_i32_e32 v5, 31, v4
	v_xor_b32_e32 v0, v4, v210
	v_lshl_add_u64 v[4:5], s[34:35], 0, v[4:5]
	v_lshlrev_b64 v[4:5], 9, v[4:5]
	v_lshlrev_b32_e32 v0, 4, v0
	v_lshl_add_u64 v[4:5], s[14:15], 0, v[4:5]
	v_and_b32_e32 v0, 0x1f0, v0
	v_lshl_add_u64 v[4:5], v[4:5], 0, v[0:1]
	v_add_u32_e32 v204, 0xc00, v210
	s_add_i32 s42, s65, 0xa000
	s_mov_b32 m0, s42
	s_nop 0
	global_load_lds_dwordx4 v[4:5], off
	v_ashrrev_i32_e32 v4, 5, v204
	v_ashrrev_i32_e32 v5, 31, v4
	v_xor_b32_e32 v0, v4, v210
	v_lshl_add_u64 v[4:5], s[34:35], 0, v[4:5]
	v_lshlrev_b64 v[4:5], 9, v[4:5]
	v_lshlrev_b32_e32 v0, 4, v0
	v_lshl_add_u64 v[4:5], s[14:15], 0, v[4:5]
	v_and_b32_e32 v0, 0x1f0, v0
	v_lshl_add_u64 v[4:5], v[4:5], 0, v[0:1]
	v_add_u32_e32 v203, 0xe00, v210
	s_add_i32 s47, s65, 0xc000
	s_mov_b32 m0, s47
	s_nop 0
	global_load_lds_dwordx4 v[4:5], off
	v_ashrrev_i32_e32 v4, 5, v203
	v_ashrrev_i32_e32 v5, 31, v4
	v_xor_b32_e32 v0, v4, v210
	v_lshl_add_u64 v[4:5], s[34:35], 0, v[4:5]
	v_lshlrev_b64 v[4:5], 9, v[4:5]
	v_lshlrev_b32_e32 v0, 4, v0
	v_bfe_u32 v180, v210, 5, 1
	v_lshlrev_b64 v[2:3], 9, v[2:3]
	v_lshl_add_u64 v[4:5], s[14:15], 0, v[4:5]
	v_and_b32_e32 v0, 0x1f0, v0
	v_lshl_add_u64 v[4:5], v[4:5], 0, v[0:1]
	v_lshl_add_u64 v[2:3], s[12:13], 0, v[2:3]
	v_lshlrev_b32_e32 v0, 4, v180
	s_add_i32 s50, s65, 0xe000
	s_mov_b32 m0, s50
	s_nop 0
	global_load_lds_dwordx4 v[4:5], off
	v_lshl_add_u64 v[162:163], v[2:3], 0, v[0:1]
	global_load_dwordx4 v[34:37], v[162:163], off
	global_load_dwordx4 v[122:125], v[162:163], off offset:32
	global_load_dwordx4 v[118:121], v[162:163], off offset:64
	global_load_dwordx4 v[114:117], v[162:163], off offset:96
	global_load_dwordx4 v[110:113], v[162:163], off offset:128
	global_load_dwordx4 v[106:109], v[162:163], off offset:160
	global_load_dwordx4 v[102:105], v[162:163], off offset:192
	global_load_dwordx4 v[98:101], v[162:163], off offset:224
	global_load_dwordx4 v[94:97], v[162:163], off offset:256
	global_load_dwordx4 v[90:93], v[162:163], off offset:288
	global_load_dwordx4 v[82:85], v[162:163], off offset:320
	global_load_dwordx4 v[86:89], v[162:163], off offset:352
	global_load_dwordx4 v[62:65], v[162:163], off offset:384
	global_load_dwordx4 v[58:61], v[162:163], off offset:416
	global_load_dwordx4 v[54:57], v[162:163], off offset:448
	global_load_dwordx4 v[50:53], v[162:163], off offset:480
	v_bfe_u32 v0, v210, 2, 7
	v_lshlrev_b32_e32 v211, 3, v210
	v_lshl_add_u64 v[2:3], s[34:35], 0, v[0:1]
	v_and_b32_e32 v127, 24, v211
	v_lshlrev_b64 v[142:143], 10, v[2:3]
	v_ashrrev_i32_e32 v170, 4, v210
	v_lshl_add_u64 v[2:3], s[18:19], 0, v[142:143]
	v_lshlrev_b32_e32 v0, 1, v127
	v_and_b32_e32 v144, 0xffffffe0, v170
	v_ashrrev_i32_e32 v168, 4, v209
	v_lshl_add_u64 v[2:3], v[2:3], 0, v[0:1]
	v_ashrrev_i32_e32 v145, 31, v144
	v_and_b32_e32 v146, 0xffffffe0, v168
	v_ashrrev_i32_e32 v166, 4, v208
	s_waitcnt vmcnt(0) lgkmcnt(0)
	s_barrier
; #define GAS __attribute__((address_space(1)))
; #define LAS __attribute__((address_space(3)))
; __device__ __forceinline__ int crow(int r, int hi) { return (r & 3) + 8 * (r >> 2) + 4 * hi; }
; #define RM_WAITBAR() asm volatile("s_waitcnt vmcnt(0) lgkmcnt(0)\n\ts_barrier" ::: "memory")
; #define RM_DMA_KS(buf) do { _Pragma("unroll") for (int i = 0; i < 8; ++i) { const int idx = tid + 512 * i, tok = idx >> 5, c = (idx & 31) ^ (tok & 31); \
;         glds16(PROJ + (size_t)T * 1024 + (hb0 + tok) * 256 + c * 8, (unsigned)__builtin_amdgcn_readfirstlane(ldsb + (buf) * 65536 + i * 8192)); } } while (0)
; #define RM_DMA_V(p, buf) do { _Pragma("unroll") for (int i = 0; i < 8; ++i) { const int idx = tid + 512 * i, tok = (idx >> 2) & 127; \
;         glds16(PROJ + (size_t)2 * T * 1024 + (hb0 + tok) * 512 + (p) * 256 + (idx >> 9) * 32 + (idx & 3) * 8, (unsigned)__builtin_amdgcn_readfirstlane(ldsb + (buf) * 65536 + i * 8192)); } } while (0)
; __device__ __forceinline__ void ret_main_phase(Frame& F, const bf16* PROJ, const bf16* ST, bf16* AO) { LTID();
;     ...
;         RM_DMA_KS(0);
;         bf16x8 pa[4][2];
;         {
;             bf16x8 qf[16];
; #pragma unroll
;             for (int s = 0; s < 16; ++s) qf[s] = *(const GAS bf16x8*)(qrow + 16 * s);
;             RM_WAITBAR();
;             asm volatile("" :: "v"(qf[0]), "v"(qf[1]), "v"(qf[2]), "v"(qf[3]), "v"(qf[4]), "v"(qf[5]), "v"(qf[6]), "v"(qf[7]), "v"(qf[8]), "v"(qf[9]), "v"(qf[10]), "v"(qf[11]), "v"(qf[12]), "v"(qf[13]), "v"(qf[14]), "v"(qf[15]));
;             RM_DMA_V(0, 1);
; #pragma unroll
;             for (int jb = 0; jb < 4; ++jb) {
;                 f32x16 S = (f32x16){0.f, 0.f, 0.f, 0.f, 0.f, 0.f, 0.f, 0.f, 0.f, 0.f, 0.f, 0.f, 0.f, 0.f, 0.f, 0.f};
;                 if (jb <= rg) {
; #pragma unroll
;                     for (int s = 0; s < 16; ++s) { const bf16x8 a = *(const LAS bf16x8*)(lds + (32 * jb + r32) * 512 + (((2 * s + hh) ^ r32) * 16)); S = __builtin_amdgcn_mfma_f32_32x32x16_bf16(a, qf[s], S, 0, 0, 0); }
;                     if (jb == rg) {
; #pragma unroll
;                         for (int i = 0; i < 16; ++i) if (crow(i, hh) > r32) S[i] = 0.f; }
	s_add_i32 s0, s65, 0x10000
	v_lshl_add_u64 v[4:5], v[144:145], 1, v[2:3]
	v_ashrrev_i32_e32 v147, 31, v146
	v_and_b32_e32 v148, 0xffffffe0, v166
	v_ashrrev_i32_e32 v164, 4, v207
	s_waitcnt vmcnt(0)
	s_mov_b32 m0, s0
	s_nop 0
	global_load_lds_dwordx4 v[4:5], off
	v_lshl_add_u64 v[4:5], v[146:147], 1, v[2:3]
	s_add_i32 s43, s65, 0x12000
	s_mov_b32 m0, s43
	s_nop 0
	global_load_lds_dwordx4 v[4:5], off
	v_ashrrev_i32_e32 v149, 31, v148
	v_and_b32_e32 v150, 0xffffffe0, v164
	v_ashrrev_i32_e32 v160, 4, v206
	v_lshl_add_u64 v[4:5], v[148:149], 1, v[2:3]
	s_add_i32 s44, s65, 0x14000
	s_mov_b32 m0, s44
	s_nop 0
	global_load_lds_dwordx4 v[4:5], off
	v_ashrrev_i32_e32 v151, 31, v150
	v_and_b32_e32 v152, 0xffffffe0, v160
	v_ashrrev_i32_e32 v158, 4, v205
	v_lshl_add_u64 v[4:5], v[150:151], 1, v[2:3]
	s_add_i32 s45, s65, 0x16000
	s_mov_b32 m0, s45
	s_nop 0
	global_load_lds_dwordx4 v[4:5], off
	v_ashrrev_i32_e32 v153, 31, v152
	v_and_b32_e32 v154, 0xffffffe0, v158
	v_ashrrev_i32_e32 v128, 4, v204
	v_ashrrev_i32_e32 v126, 4, v203
	v_lshl_add_u64 v[4:5], v[152:153], 1, v[2:3]
	s_add_i32 s51, s65, 0x18000
	s_mov_b32 m0, s51
	s_nop 0
	global_load_lds_dwordx4 v[4:5], off
	v_ashrrev_i32_e32 v155, 31, v154
	v_and_b32_e32 v156, 0xffffffe0, v128
	v_and_b32_e32 v172, 0xffffffe0, v126
	v_lshl_add_u64 v[4:5], v[154:155], 1, v[2:3]
	s_add_i32 s56, s65, 0x1a000
	s_mov_b32 m0, s56
	s_nop 0
	global_load_lds_dwordx4 v[4:5], off
	v_ashrrev_i32_e32 v157, 31, v156
	v_ashrrev_i32_e32 v173, 31, v172
	v_lshrrev_b32_e32 v6, 5, v210
	v_lshl_add_u64 v[4:5], v[156:157], 1, v[2:3]
	s_add_i32 s62, s65, 0x1c000
	s_mov_b32 m0, s62
	s_nop 0
	global_load_lds_dwordx4 v[4:5], off
	v_lshl_add_u64 v[2:3], v[172:173], 1, v[2:3]
	s_add_i32 s63, s65, 0x1e000
	s_mov_b32 m0, s63
	s_nop 0
	global_load_lds_dwordx4 v[2:3], off
	v_bitop3_b32 v2, v6, v213, 1 bitop3:0x6c
	v_lshl_add_u32 v22, v213, 9, 0
	v_lshlrev_b32_e32 v2, 4, v2
	v_add_u32_e32 v38, v22, v2
	ds_read_b128 v[2:5], v38
	v_bitop3_b32 v18, v180, v213, 2 bitop3:0x36
	v_lshlrev_b32_e32 v18, 4, v18
	v_add_u32_e32 v39, v22, v18
	ds_read_b128 v[18:21], v39
	s_waitcnt lgkmcnt(1)
	v_mfma_f32_32x32x16_bf16 v[2:17], v[2:5], v[34:37], 0
	s_cmp_lg_u32 s66, 0
	s_cselect_b64 s[8:9], -1, 0
	v_lshlrev_b32_e32 v214, 2, v180
	s_and_b64 vcc, exec, s[8:9]
	s_waitcnt lgkmcnt(0)
	v_mfma_f32_32x32x16_bf16 v[2:17], v[18:21], v[122:125], v[2:17]
	v_bitop3_b32 v18, v180, v213, 4 bitop3:0x36
	v_lshlrev_b32_e32 v18, 4, v18
	v_add_u32_e32 v129, v22, v18
	ds_read_b128 v[18:21], v129
	s_waitcnt lgkmcnt(0)
	v_mfma_f32_32x32x16_bf16 v[2:17], v[18:21], v[118:121], v[2:17]
	v_bitop3_b32 v18, v180, v213, 6 bitop3:0x36
	v_lshlrev_b32_e32 v18, 4, v18
	v_add_u32_e32 v130, v22, v18
	ds_read_b128 v[18:21], v130
	s_waitcnt lgkmcnt(0)
	v_mfma_f32_32x32x16_bf16 v[2:17], v[18:21], v[114:117], v[2:17]
	v_bitop3_b32 v18, v180, v213, 8 bitop3:0x36
	v_lshlrev_b32_e32 v18, 4, v18
	v_add_u32_e32 v131, v22, v18
	ds_read_b128 v[18:21], v131
	s_waitcnt lgkmcnt(0)
	v_mfma_f32_32x32x16_bf16 v[2:17], v[18:21], v[110:113], v[2:17]
	v_bitop3_b32 v18, v180, v213, 10 bitop3:0x36
	v_lshlrev_b32_e32 v18, 4, v18
	v_add_u32_e32 v132, v22, v18
	ds_read_b128 v[18:21], v132
	s_waitcnt lgkmcnt(0)
	v_mfma_f32_32x32x16_bf16 v[2:17], v[18:21], v[106:109], v[2:17]
	v_bitop3_b32 v18, v180, v213, 12 bitop3:0x36
	v_lshlrev_b32_e32 v18, 4, v18
	v_add_u32_e32 v133, v22, v18
	ds_read_b128 v[18:21], v133
	s_waitcnt lgkmcnt(0)
	v_mfma_f32_32x32x16_bf16 v[2:17], v[18:21], v[102:105], v[2:17]
	v_bitop3_b32 v18, v180, v213, 14 bitop3:0x36
	v_lshlrev_b32_e32 v18, 4, v18
	v_add_u32_e32 v134, v22, v18
	ds_read_b128 v[18:21], v134
	s_waitcnt lgkmcnt(0)
	v_mfma_f32_32x32x16_bf16 v[2:17], v[18:21], v[98:101], v[2:17]
	v_bitop3_b32 v18, v180, v213, 16 bitop3:0x36
	v_lshlrev_b32_e32 v18, 4, v18
	v_add_u32_e32 v135, v22, v18
	ds_read_b128 v[18:21], v135
	s_waitcnt lgkmcnt(0)
	v_mfma_f32_32x32x16_bf16 v[2:17], v[18:21], v[94:97], v[2:17]
	v_bitop3_b32 v18, v180, v213, 18 bitop3:0x36
	v_lshlrev_b32_e32 v18, 4, v18
	v_add_u32_e32 v136, v22, v18
	ds_read_b128 v[18:21], v136
	s_waitcnt lgkmcnt(0)
	v_mfma_f32_32x32x16_bf16 v[2:17], v[18:21], v[90:93], v[2:17]
	v_bitop3_b32 v18, v180, v213, 20 bitop3:0x36
	v_lshlrev_b32_e32 v18, 4, v18
	v_add_u32_e32 v137, v22, v18
	ds_read_b128 v[18:21], v137
	s_waitcnt lgkmcnt(0)
	v_mfma_f32_32x32x16_bf16 v[2:17], v[18:21], v[82:85], v[2:17]
	v_bitop3_b32 v18, v180, v213, 22 bitop3:0x36
	v_lshlrev_b32_e32 v18, 4, v18
	v_add_u32_e32 v138, v22, v18
	ds_read_b128 v[18:21], v138
	s_waitcnt lgkmcnt(0)
	v_mfma_f32_32x32x16_bf16 v[2:17], v[18:21], v[86:89], v[2:17]
	v_bitop3_b32 v18, v180, v213, 24 bitop3:0x36
	v_lshlrev_b32_e32 v18, 4, v18
	v_add_u32_e32 v139, v22, v18
	ds_read_b128 v[18:21], v139
	s_waitcnt lgkmcnt(0)
	v_mfma_f32_32x32x16_bf16 v[2:17], v[18:21], v[62:65], v[2:17]
	v_bitop3_b32 v18, v180, v213, 26 bitop3:0x36
	v_lshlrev_b32_e32 v18, 4, v18
	v_add_u32_e32 v140, v22, v18
	ds_read_b128 v[18:21], v140
	s_waitcnt lgkmcnt(0)
	v_mfma_f32_32x32x16_bf16 v[2:17], v[18:21], v[58:61], v[2:17]
	v_bitop3_b32 v18, v180, v213, 28 bitop3:0x36
	v_lshlrev_b32_e32 v18, 4, v18
	v_add_u32_e32 v141, v22, v18
	ds_read_b128 v[18:21], v141
	s_waitcnt lgkmcnt(0)
	v_mfma_f32_32x32x16_bf16 v[2:17], v[18:21], v[54:57], v[2:17]
	v_bitop3_b32 v18, v180, v213, 30 bitop3:0x36
	v_lshlrev_b32_e32 v18, 4, v18
	v_add_u32_e32 v159, v22, v18
	ds_read_b128 v[18:21], v159
	s_waitcnt lgkmcnt(0)
	v_mfma_f32_32x32x16_bf16 v[2:17], v[18:21], v[50:53], v[2:17]
	s_cbranch_vccnz .LBB0_367
; __device__ __forceinline__ int crow(int r, int hi) { return (r & 3) + 8 * (r >> 2) + 4 * hi; }
; __device__ __forceinline__ void ret_main_phase(Frame& F, const bf16* PROJ, const bf16* ST, bf16* AO) { LTID();
;     ...
;                     if (jb == rg) {
; #pragma unroll
;                         for (int i = 0; i < 16; ++i) if (crow(i, hh) > r32) S[i] = 0.f; }
	v_cmp_lt_u32_e32 vcc, v214, v213
	v_or_b32_e32 v18, 2, v214
	s_nop 8
	v_cndmask_b32_e32 v3, 0, v3, vcc
	v_cmp_le_u32_e32 vcc, v214, v213
	s_nop 1
	v_cndmask_b32_e32 v2, 0, v2, vcc
	v_cmp_le_u32_e32 vcc, v18, v213
	v_or_b32_e32 v18, 3, v214
	s_nop 0
	v_cndmask_b32_e32 v4, 0, v4, vcc
	v_cmp_le_u32_e32 vcc, v18, v213
	v_or_b32_e32 v18, 8, v214
	s_nop 0
	v_cndmask_b32_e32 v5, 0, v5, vcc
	v_cmp_le_u32_e32 vcc, v18, v213
	v_or_b32_e32 v18, 9, v214
	s_nop 0
	v_cndmask_b32_e32 v6, 0, v6, vcc
	v_cmp_le_u32_e32 vcc, v18, v213
	v_or_b32_e32 v18, 10, v214
	s_nop 0
	v_cndmask_b32_e32 v7, 0, v7, vcc
	v_cmp_le_u32_e32 vcc, v18, v213
	v_or_b32_e32 v18, 11, v214
	s_nop 0
	v_cndmask_b32_e32 v8, 0, v8, vcc
	v_cmp_le_u32_e32 vcc, v18, v213
	v_or_b32_e32 v18, 16, v214
	s_nop 0
	v_cndmask_b32_e32 v9, 0, v9, vcc
	v_cmp_le_u32_e32 vcc, v18, v213
	v_or_b32_e32 v18, 17, v214
	s_nop 0
	v_cndmask_b32_e32 v10, 0, v10, vcc
	v_cmp_le_u32_e32 vcc, v18, v213
	v_or_b32_e32 v18, 18, v214
	s_nop 0
	v_cndmask_b32_e32 v11, 0, v11, vcc
	v_cmp_le_u32_e32 vcc, v18, v213
	v_or_b32_e32 v18, 19, v214
	s_nop 0
	v_cndmask_b32_e32 v12, 0, v12, vcc
	v_cmp_le_u32_e32 vcc, v18, v213
	v_or_b32_e32 v18, 24, v214
	s_nop 0
	v_cndmask_b32_e32 v13, 0, v13, vcc
	v_cmp_le_u32_e32 vcc, v18, v213
	v_or_b32_e32 v18, 25, v214
	s_nop 0
	v_cndmask_b32_e32 v14, 0, v14, vcc
	v_cmp_le_u32_e32 vcc, v18, v213
	v_or_b32_e32 v18, 26, v214
	s_nop 0
	v_cndmask_b32_e32 v15, 0, v15, vcc
	v_cmp_le_u32_e32 vcc, v18, v213
	v_or_b32_e32 v18, 27, v214
	s_nop 0
	v_cndmask_b32_e32 v16, 0, v16, vcc
	v_cmp_le_u32_e32 vcc, v18, v213
	s_nop 1
	v_cndmask_b32_e32 v17, 0, v17, vcc

; #define RM_WAITBAR() asm volatile("s_waitcnt vmcnt(0) lgkmcnt(0)\n\ts_barrier" ::: "memory")
; #define RM_DMA_V(p, buf) do { _Pragma("unroll") for (int i = 0; i < 8; ++i) { const int idx = tid + 512 * i, tok = (idx >> 2) & 127; \
;         glds16(PROJ + (size_t)2 * T * 1024 + (hb0 + tok) * 512 + (p) * 256 + (idx >> 9) * 32 + (idx & 3) * 8, (unsigned)__builtin_amdgcn_readfirstlane(ldsb + (buf) * 65536 + i * 8192)); } } while (0)
; __device__ __forceinline__ void ret_main_phase(Frame& F, const bf16* PROJ, const bf16* ST, bf16* AO) { LTID();
;     ...
;                 pa[jb][0] = pack8f(S[0], S[1], S[2], S[3], S[4], S[5], S[6], S[7]); pa[jb][1] = pack8f(S[8], S[9], S[10], S[11], S[12], S[13], S[14], S[15]);
;             }
;         }
;         f32x16 o[8];
; #pragma unroll
;         for (int eb = 0; eb < 8; ++eb) o[eb] = (f32x16){0.f, 0.f, 0.f, 0.f, 0.f, 0.f, 0.f, 0.f, 0.f, 0.f, 0.f, 0.f, 0.f, 0.f, 0.f, 0.f};
;     ...
;         bf16x8 qa[8];
;         RM_WAITBAR(); RM_DMA_V(1, 0);      RM_PV(1, 0);
.LBB0_375:
	v_lshlrev_b32_e32 v212, 4, v210
	v_cvt_pk_bf16_f32 v114, v2, v3
	v_and_b32_e32 v2, 0xc0, v212
	v_lshlrev_b32_e32 v3, 1, v210
	v_and_b32_e32 v3, 32, v3
	v_lshl_or_b32 v2, v180, 8, v2
	v_cvt_pk_bf16_f32 v116, v6, v7
	v_or3_b32 v6, v2, v3, v127
	v_lshl_add_u64 v[2:3], s[12:13], 0, v[142:143]
	v_lshl_add_u64 v[2:3], v[2:3], 0, v[0:1]
	s_mov_b64 s[8:9], 0x8000200
	s_waitcnt vmcnt(0) lgkmcnt(0)
	s_barrier
	v_lshl_add_u64 v[2:3], v[2:3], 0, s[8:9]
	v_cvt_pk_bf16_f32 v115, v4, v5
	v_lshl_add_u64 v[4:5], v[144:145], 1, v[2:3]
	s_mov_b32 m0, s65
	s_nop 0
	global_load_lds_dwordx4 v[4:5], off
	v_lshl_add_u64 v[4:5], v[146:147], 1, v[2:3]
	s_mov_b32 m0, s68
	s_nop 0
	global_load_lds_dwordx4 v[4:5], off
	v_lshl_add_u64 v[4:5], v[148:149], 1, v[2:3]
	s_mov_b32 m0, s69
	s_nop 0
	global_load_lds_dwordx4 v[4:5], off
	v_lshl_add_u64 v[4:5], v[150:151], 1, v[2:3]
	s_mov_b32 m0, s70
	s_nop 0
	global_load_lds_dwordx4 v[4:5], off
	v_lshl_add_u64 v[4:5], v[152:153], 1, v[2:3]
	s_mov_b32 m0, s46
	s_nop 0
	global_load_lds_dwordx4 v[4:5], off
	v_lshl_add_u64 v[4:5], v[154:155], 1, v[2:3]
	s_mov_b32 m0, s42
	s_nop 0
	global_load_lds_dwordx4 v[4:5], off
	v_lshl_add_u64 v[4:5], v[156:157], 1, v[2:3]
	s_mov_b32 m0, s47
	s_nop 0
	global_load_lds_dwordx4 v[4:5], off
	s_ashr_i32 s66, s61, 8
	v_lshl_add_u64 v[2:3], v[172:173], 1, v[2:3]
	s_mov_b32 m0, s50
	s_nop 0
	global_load_lds_dwordx4 v[2:3], off
	s_lshl_b32 s2, s66, 15
	s_add_i32 s67, s2, 0
	v_add_u32_e32 v181, s67, v6
	v_add_u32_e32 v0, 0x10000, v181
	v_cvt_pk_bf16_f32 v134, v18, v19
	v_cvt_pk_bf16_f32 v135, v20, v21
	v_cvt_pk_bf16_f32 v117, v8, v9
	ds_read_b64_tr_b16 v[2:3], v0
	ds_read_b64_tr_b16 v[4:5], v0 offset:512
	ds_read_b64_tr_b16 v[18:19], v0 offset:8192
	ds_read_b64_tr_b16 v[20:21], v0 offset:8704
	ds_read_b64_tr_b16 v[34:35], v0 offset:16384
	ds_read_b64_tr_b16 v[36:37], v0 offset:16896
	ds_read_b64_tr_b16 v[50:51], v0 offset:24576
	ds_read_b64_tr_b16 v[52:53], v0 offset:25088
	v_cvt_pk_bf16_f32 v136, v22, v23
	v_cvt_pk_bf16_f32 v137, v24, v25
	v_cvt_pk_bf16_f32 v130, v26, v27
	v_cvt_pk_bf16_f32 v131, v28, v29
	v_cvt_pk_bf16_f32 v132, v30, v31
	v_cvt_pk_bf16_f32 v133, v32, v33
	v_cvt_pk_bf16_f32 v138, v10, v11
	v_cvt_pk_bf16_f32 v139, v12, v13
	v_cvt_pk_bf16_f32 v140, v14, v15
	v_cvt_pk_bf16_f32 v141, v16, v17
	s_waitcnt lgkmcnt(6)
	v_mfma_f32_32x32x16_bf16 v[2:17], v[114:117], v[2:5], 0
	s_waitcnt lgkmcnt(4)
	v_mfma_f32_32x32x16_bf16 v[18:33], v[114:117], v[18:21], 0
	s_waitcnt lgkmcnt(2)
	v_mfma_f32_32x32x16_bf16 v[34:49], v[114:117], v[34:37], 0
	s_waitcnt lgkmcnt(0)
	v_mfma_f32_32x32x16_bf16 v[50:65], v[114:117], v[50:53], 0
	ds_read_b64_tr_b16 v[82:83], v0 offset:1024
	ds_read_b64_tr_b16 v[84:85], v0 offset:1536
	s_waitcnt lgkmcnt(0)
	v_mfma_f32_32x32x16_bf16 v[2:17], v[138:141], v[82:85], v[2:17]
	ds_read_b64_tr_b16 v[82:83], v0 offset:9216
	ds_read_b64_tr_b16 v[84:85], v0 offset:9728
	s_waitcnt lgkmcnt(0)
	v_mfma_f32_32x32x16_bf16 v[18:33], v[138:141], v[82:85], v[18:33]
	ds_read_b64_tr_b16 v[82:83], v0 offset:17408
	ds_read_b64_tr_b16 v[84:85], v0 offset:17920
	s_waitcnt lgkmcnt(0)
	v_mfma_f32_32x32x16_bf16 v[34:49], v[138:141], v[82:85], v[34:49]
	ds_read_b64_tr_b16 v[82:83], v0 offset:25600
	ds_read_b64_tr_b16 v[84:85], v0 offset:26112
	s_waitcnt lgkmcnt(0)
	v_mfma_f32_32x32x16_bf16 v[50:65], v[138:141], v[82:85], v[50:65]
	s_and_b64 vcc, exec, s[6:7]
	s_cbranch_vccnz .LBB0_377
	ds_read_b64_tr_b16 v[82:83], v0 offset:2048
	ds_read_b64_tr_b16 v[84:85], v0 offset:2560
	s_waitcnt lgkmcnt(0)
	v_mfma_f32_32x32x16_bf16 v[2:17], v[134:137], v[82:85], v[2:17]
	ds_read_b64_tr_b16 v[82:83], v0 offset:10240
	ds_read_b64_tr_b16 v[84:85], v0 offset:10752
	s_waitcnt lgkmcnt(0)
	v_mfma_f32_32x32x16_bf16 v[18:33], v[134:137], v[82:85], v[18:33]
	ds_read_b64_tr_b16 v[82:83], v0 offset:18432
	ds_read_b64_tr_b16 v[84:85], v0 offset:18944
	s_waitcnt lgkmcnt(0)
	v_mfma_f32_32x32x16_bf16 v[34:49], v[134:137], v[82:85], v[34:49]
	ds_read_b64_tr_b16 v[82:83], v0 offset:26624
	ds_read_b64_tr_b16 v[84:85], v0 offset:27136
	s_waitcnt lgkmcnt(0)
	v_mfma_f32_32x32x16_bf16 v[50:65], v[134:137], v[82:85], v[50:65]
	ds_read_b64_tr_b16 v[82:83], v0 offset:3072
	ds_read_b64_tr_b16 v[84:85], v0 offset:3584
	s_waitcnt lgkmcnt(0)
	v_mfma_f32_32x32x16_bf16 v[2:17], v[130:133], v[82:85], v[2:17]
	ds_read_b64_tr_b16 v[82:83], v0 offset:11264
	ds_read_b64_tr_b16 v[84:85], v0 offset:11776
	s_waitcnt lgkmcnt(0)
	v_mfma_f32_32x32x16_bf16 v[18:33], v[130:133], v[82:85], v[18:33]
	ds_read_b64_tr_b16 v[82:83], v0 offset:19456
	ds_read_b64_tr_b16 v[84:85], v0 offset:19968
	s_waitcnt lgkmcnt(0)
	v_mfma_f32_32x32x16_bf16 v[34:49], v[130:133], v[82:85], v[34:49]
	ds_read_b64_tr_b16 v[82:83], v0 offset:27648
	ds_read_b64_tr_b16 v[84:85], v0 offset:28160
	s_waitcnt lgkmcnt(0)
	v_mfma_f32_32x32x16_bf16 v[50:65], v[130:133], v[82:85], v[50:65]

; #define RM_WAITBAR() asm volatile("s_waitcnt vmcnt(0) lgkmcnt(0)\n\ts_barrier" ::: "memory")
; #define RM_DMA_V(p, buf) do { _Pragma("unroll") for (int i = 0; i < 8; ++i) { const int idx = tid + 512 * i, tok = (idx >> 2) & 127; \
;         glds16(PROJ + (size_t)2 * T * 1024 + (hb0 + tok) * 512 + (p) * 256 + (idx >> 9) * 32 + (idx & 3) * 8, (unsigned)__builtin_amdgcn_readfirstlane(ldsb + (buf) * 65536 + i * 8192)); } } while (0)
; #define RM_DMA_ST(p, dkh, buf) do { _Pragma("unroll") for (int i = 0; i < 8; ++i) { const int idx = tid + 512 * i, e = idx >> 4, c = (idx & 15) ^ (e & 15); \
;         glds16(stb + (size_t)((p) * 256 + e) * 256 + (dkh) * 128 + c * 8, (unsigned)__builtin_amdgcn_readfirstlane(ldsb + (buf) * 65536 + i * 8192)); } } while (0)
; __device__ __forceinline__ void ret_main_phase(Frame& F, const bf16* PROJ, const bf16* ST, bf16* AO) { LTID();
;     ...
;         bf16x8 qa[8];
;         RM_WAITBAR(); RM_DMA_V(1, 0);      RM_PV(1, 0);
;         RM_WAITBAR(); RM_DMA_ST(0, 0, 1);  RM_PV(0, 4);
.LBB0_381:
	v_xor_b32_e32 v0, v170, v210
	v_ashrrev_i32_e32 v171, 31, v170
	v_lshlrev_b32_e32 v0, 3, v0
	v_lshlrev_b64 v[66:67], 9, v[170:171]
	v_and_b32_e32 v0, 0x78, v0
	v_lshl_add_u64 v[196:197], s[28:29], 0, v[66:67]
	v_lshlrev_b32_e32 v0, 1, v0
	s_waitcnt vmcnt(0) lgkmcnt(0)
	s_barrier
	v_lshl_add_u64 v[66:67], v[196:197], 0, v[0:1]
	v_ashrrev_i32_e32 v169, 31, v168
	s_mov_b32 m0, s0
	s_nop 0
	global_load_lds_dwordx4 v[66:67], off
	v_xor_b32_e32 v68, v168, v210
	v_lshlrev_b64 v[66:67], 9, v[168:169]
	v_lshl_add_u64 v[198:199], s[28:29], 0, v[66:67]
	v_lshlrev_b32_e32 v66, 3, v68
	v_and_b32_e32 v66, 0x78, v66
	v_lshlrev_b32_e32 v200, 1, v66
	v_mov_b32_e32 v201, v1
	v_lshl_add_u64 v[66:67], v[198:199], 0, v[200:201]
	v_ashrrev_i32_e32 v167, 31, v166
	s_mov_b32 m0, s43
	s_nop 0
	global_load_lds_dwordx4 v[66:67], off
	v_xor_b32_e32 v68, v166, v210
	v_lshlrev_b64 v[66:67], 9, v[166:167]
	v_lshl_add_u64 v[168:169], s[28:29], 0, v[66:67]
	v_lshlrev_b32_e32 v66, 3, v68
	v_and_b32_e32 v66, 0x78, v66
	v_lshlrev_b32_e32 v194, 1, v66
	v_mov_b32_e32 v195, v1
	v_lshl_add_u64 v[66:67], v[168:169], 0, v[194:195]
	v_ashrrev_i32_e32 v165, 31, v164
	s_mov_b32 m0, s44
	s_nop 0
	global_load_lds_dwordx4 v[66:67], off
	v_xor_b32_e32 v68, v164, v210
	v_lshlrev_b64 v[66:67], 9, v[164:165]
	v_lshl_add_u64 v[170:171], s[28:29], 0, v[66:67]
	v_lshlrev_b32_e32 v66, 3, v68
	v_and_b32_e32 v66, 0x78, v66
	v_lshlrev_b32_e32 v192, 1, v66
	v_mov_b32_e32 v193, v1
	v_lshl_add_u64 v[66:67], v[170:171], 0, v[192:193]
	v_ashrrev_i32_e32 v161, 31, v160
	s_mov_b32 m0, s45
	s_nop 0
	global_load_lds_dwordx4 v[66:67], off
	v_xor_b32_e32 v68, v160, v210
	v_lshlrev_b64 v[66:67], 9, v[160:161]
	v_lshl_add_u64 v[172:173], s[28:29], 0, v[66:67]
	v_lshlrev_b32_e32 v66, 3, v68
	v_and_b32_e32 v66, 0x78, v66
	v_lshlrev_b32_e32 v190, 1, v66
	v_mov_b32_e32 v191, v1
	v_lshl_add_u64 v[66:67], v[172:173], 0, v[190:191]
	v_ashrrev_i32_e32 v159, 31, v158
	s_mov_b32 m0, s51
	s_nop 0
	global_load_lds_dwordx4 v[66:67], off
	v_xor_b32_e32 v68, v158, v210
	v_lshlrev_b64 v[66:67], 9, v[158:159]
	v_lshl_add_u64 v[174:175], s[28:29], 0, v[66:67]
	v_lshlrev_b32_e32 v66, 3, v68
	v_and_b32_e32 v66, 0x78, v66
	v_lshlrev_b32_e32 v188, 1, v66
	v_mov_b32_e32 v189, v1
	v_lshl_add_u64 v[66:67], v[174:175], 0, v[188:189]
	v_ashrrev_i32_e32 v129, 31, v128
	s_mov_b32 m0, s56
	s_nop 0
	global_load_lds_dwordx4 v[66:67], off
	v_xor_b32_e32 v68, v128, v210
	v_lshlrev_b64 v[66:67], 9, v[128:129]
	v_lshl_add_u64 v[176:177], s[28:29], 0, v[66:67]
	v_lshlrev_b32_e32 v66, 3, v68
	v_and_b32_e32 v66, 0x78, v66
	v_lshlrev_b32_e32 v186, 1, v66
	v_mov_b32_e32 v187, v1
	v_lshl_add_u64 v[66:67], v[176:177], 0, v[186:187]
	v_ashrrev_i32_e32 v127, 31, v126
	s_mov_b32 m0, s62
	s_nop 0
	global_load_lds_dwordx4 v[66:67], off
	v_xor_b32_e32 v68, v126, v210
	v_lshlrev_b64 v[66:67], 9, v[126:127]
	v_lshl_add_u64 v[178:179], s[28:29], 0, v[66:67]
	v_lshlrev_b32_e32 v66, 3, v68
	v_and_b32_e32 v66, 0x78, v66
	v_lshlrev_b32_e32 v184, 1, v66
	v_mov_b32_e32 v185, v1
	v_lshl_add_u64 v[66:67], v[178:179], 0, v[184:185]
	s_mov_b32 m0, s63
	s_nop 0
	global_load_lds_dwordx4 v[66:67], off
	ds_read_b64_tr_b16 v[66:67], v181
	ds_read_b64_tr_b16 v[68:69], v181 offset:512
	ds_read_b64_tr_b16 v[82:83], v181 offset:8192
	ds_read_b64_tr_b16 v[84:85], v181 offset:8704
	ds_read_b64_tr_b16 v[98:99], v181 offset:16384
	ds_read_b64_tr_b16 v[100:101], v181 offset:16896
	ds_read_b64_tr_b16 v[118:119], v181 offset:24576
	ds_read_b64_tr_b16 v[120:121], v181 offset:25088
	s_waitcnt lgkmcnt(6)
	v_mfma_f32_32x32x16_bf16 v[66:81], v[114:117], v[66:69], 0
	s_waitcnt lgkmcnt(4)
	v_mfma_f32_32x32x16_bf16 v[82:97], v[114:117], v[82:85], 0
	s_waitcnt lgkmcnt(2)
	v_mfma_f32_32x32x16_bf16 v[98:113], v[114:117], v[98:101], 0
	s_waitcnt lgkmcnt(0)
	v_mfma_f32_32x32x16_bf16 v[114:129], v[114:117], v[118:121], 0
	ds_read_b64_tr_b16 v[158:159], v181 offset:1024
	ds_read_b64_tr_b16 v[160:161], v181 offset:1536
	s_waitcnt lgkmcnt(0)
	v_mfma_f32_32x32x16_bf16 v[66:81], v[138:141], v[158:161], v[66:81]
	ds_read_b64_tr_b16 v[158:159], v181 offset:9216
	ds_read_b64_tr_b16 v[160:161], v181 offset:9728
	s_waitcnt lgkmcnt(0)
	v_mfma_f32_32x32x16_bf16 v[82:97], v[138:141], v[158:161], v[82:97]
	ds_read_b64_tr_b16 v[158:159], v181 offset:17408
	ds_read_b64_tr_b16 v[160:161], v181 offset:17920
	s_waitcnt lgkmcnt(0)
	v_mfma_f32_32x32x16_bf16 v[98:113], v[138:141], v[158:161], v[98:113]
	ds_read_b64_tr_b16 v[158:159], v181 offset:25600
	ds_read_b64_tr_b16 v[160:161], v181 offset:26112
	s_waitcnt lgkmcnt(0)
	v_mfma_f32_32x32x16_bf16 v[114:129], v[138:141], v[158:161], v[114:129]
	s_and_b64 vcc, exec, s[6:7]
	s_cbranch_vccnz .LBB0_417
	ds_read_b64_tr_b16 v[138:139], v181 offset:2048
	ds_read_b64_tr_b16 v[140:141], v181 offset:2560
	s_waitcnt lgkmcnt(0)
	v_mfma_f32_32x32x16_bf16 v[66:81], v[134:137], v[138:141], v[66:81]
	ds_read_b64_tr_b16 v[138:139], v181 offset:10240
	ds_read_b64_tr_b16 v[140:141], v181 offset:10752
	s_waitcnt lgkmcnt(0)
	v_mfma_f32_32x32x16_bf16 v[82:97], v[134:137], v[138:141], v[82:97]
	ds_read_b64_tr_b16 v[138:139], v181 offset:18432
	ds_read_b64_tr_b16 v[140:141], v181 offset:18944
	s_waitcnt lgkmcnt(0)
	v_mfma_f32_32x32x16_bf16 v[98:113], v[134:137], v[138:141], v[98:113]
	ds_read_b64_tr_b16 v[138:139], v181 offset:26624
	ds_read_b64_tr_b16 v[140:141], v181 offset:27136
	s_waitcnt lgkmcnt(0)
	v_mfma_f32_32x32x16_bf16 v[114:129], v[134:137], v[138:141], v[114:129]
	ds_read_b64_tr_b16 v[134:135], v181 offset:3072
	ds_read_b64_tr_b16 v[136:137], v181 offset:3584
	s_waitcnt lgkmcnt(0)
	v_mfma_f32_32x32x16_bf16 v[66:81], v[130:133], v[134:137], v[66:81]
	ds_read_b64_tr_b16 v[134:135], v181 offset:11264
	ds_read_b64_tr_b16 v[136:137], v181 offset:11776
	s_waitcnt lgkmcnt(0)
	v_mfma_f32_32x32x16_bf16 v[82:97], v[130:133], v[134:137], v[82:97]
	ds_read_b64_tr_b16 v[134:135], v181 offset:19456
	ds_read_b64_tr_b16 v[136:137], v181 offset:19968
	s_waitcnt lgkmcnt(0)
	v_mfma_f32_32x32x16_bf16 v[98:113], v[130:133], v[134:137], v[98:113]
	ds_read_b64_tr_b16 v[134:135], v181 offset:27648
	ds_read_b64_tr_b16 v[136:137], v181 offset:28160
	s_waitcnt lgkmcnt(0)
	v_mfma_f32_32x32x16_bf16 v[114:129], v[130:133], v[134:137], v[114:129]
	s_and_b64 vcc, exec, s[8:9]
	s_cbranch_vccz .LBB0_418

; #define RM_WAITBAR() asm volatile("s_waitcnt vmcnt(0) lgkmcnt(0)\n\ts_barrier" ::: "memory")
; #define RM_DMA_V(p, buf) do { _Pragma("unroll") for (int i = 0; i < 8; ++i) { const int idx = tid + 512 * i, tok = (idx >> 2) & 127; \
;         glds16(PROJ + (size_t)2 * T * 1024 + (hb0 + tok) * 512 + (p) * 256 + (idx >> 9) * 32 + (idx & 3) * 8, (unsigned)__builtin_amdgcn_readfirstlane(ldsb + (buf) * 65536 + i * 8192)); } } while (0)
; #define RM_DMA_ST(p, dkh, buf) do { _Pragma("unroll") for (int i = 0; i < 8; ++i) { const int idx = tid + 512 * i, e = idx >> 4, c = (idx & 15) ^ (e & 15); \
;         glds16(stb + (size_t)((p) * 256 + e) * 256 + (dkh) * 128 + c * 8, (unsigned)__builtin_amdgcn_readfirstlane(ldsb + (buf) * 65536 + i * 8192)); } } while (0)
; #define RM_QA(DKH) do { _Pragma("unroll") for (int sl = 0; sl < 8; ++sl) qa[sl] = *(const GAS bf16x8*)(qrow + 16 * ((DKH) * 8 + sl)); } while (0)
; #define RM_QA_USE() asm volatile("" :: "v"(qa[0]), "v"(qa[1]), "v"(qa[2]), "v"(qa[3]), "v"(qa[4]), "v"(qa[5]), "v"(qa[6]), "v"(qa[7]))
; __device__ __forceinline__ void ret_main_phase(Frame& F, const bf16* PROJ, const bf16* ST, bf16* AO) { LTID();
;     ...
;         bf16x8 qa[8];
;         RM_WAITBAR(); RM_DMA_V(1, 0);      RM_PV(1, 0);
;         RM_WAITBAR(); RM_DMA_ST(0, 0, 1);  RM_PV(0, 4);
;         RM_QA(0); RM_WAITBAR(); RM_QA_USE(); RM_DMA_ST(0, 1, 0);  RM_CROSS(1, 0);
;         RM_QA(1); RM_WAITBAR(); RM_QA_USE(); RM_DMA_ST(1, 0, 1);  RM_CROSS(0, 0);
.LBB0_385:
	global_load_dwordx4 v[158:161], v[162:163], off
	global_load_dwordx4 v[154:157], v[162:163], off offset:32
	global_load_dwordx4 v[150:153], v[162:163], off offset:64
	global_load_dwordx4 v[146:149], v[162:163], off offset:96
	global_load_dwordx4 v[142:145], v[162:163], off offset:128
	global_load_dwordx4 v[138:141], v[162:163], off offset:160
	global_load_dwordx4 v[134:137], v[162:163], off offset:192
	global_load_dwordx4 v[130:133], v[162:163], off offset:224
	v_lshl_add_u64 v[164:165], v[196:197], 0, v[0:1]
	v_lshl_add_u64 v[166:167], v[164:165], 0, s[16:17]
	v_mov_b32_e32 v201, v1
	s_waitcnt vmcnt(0) lgkmcnt(0)
	s_barrier
	v_mov_b32_e32 v195, v1
	v_lshl_add_u64 v[168:169], v[168:169], 0, v[194:195]
	v_mov_b32_e32 v193, v1
	v_lshl_add_u64 v[170:171], v[170:171], 0, v[192:193]
	v_mov_b32_e32 v191, v1
	v_lshl_add_u64 v[172:173], v[172:173], 0, v[190:191]
	v_mov_b32_e32 v189, v1
	v_lshl_add_u64 v[174:175], v[174:175], 0, v[188:189]
	v_mov_b32_e32 v187, v1
	v_lshl_add_u64 v[176:177], v[176:177], 0, v[186:187]
	v_mov_b32_e32 v185, v1
	v_lshl_add_u64 v[178:179], v[178:179], 0, v[184:185]
	v_or_b32_e32 v215, 2, v180
	v_or_b32_e32 v216, 4, v180
	v_or_b32_e32 v217, 6, v180
	v_or_b32_e32 v218, 8, v180
	v_or_b32_e32 v219, 10, v180
	v_or_b32_e32 v220, 12, v180
	v_or_b32_e32 v181, 14, v180
	v_bitop3_b32 v180, v180, v210, 15 bitop3:0x78
	v_lshlrev_b32_e32 v0, 8, v213
	v_lshlrev_b32_e32 v221, 4, v180
	s_waitcnt vmcnt(0)
	s_mov_b32 m0, s65
	s_nop 0
	global_load_lds_dwordx4 v[166:167], off
	v_lshl_add_u64 v[166:167], v[198:199], 0, v[200:201]
	v_lshl_add_u64 v[182:183], v[166:167], 0, s[16:17]
	s_mov_b32 m0, s68
	s_nop 0
	global_load_lds_dwordx4 v[182:183], off
	v_lshl_add_u64 v[182:183], v[168:169], 0, s[16:17]
	s_mov_b32 m0, s69
	s_nop 0
	global_load_lds_dwordx4 v[182:183], off
	v_lshl_add_u64 v[182:183], v[170:171], 0, s[16:17]
	s_mov_b32 m0, s70
	s_nop 0
	global_load_lds_dwordx4 v[182:183], off
	v_lshl_add_u64 v[182:183], v[172:173], 0, s[16:17]
	s_mov_b32 m0, s46
	s_nop 0
	global_load_lds_dwordx4 v[182:183], off
	v_lshl_add_u64 v[182:183], v[174:175], 0, s[16:17]
	s_mov_b32 m0, s42
	s_nop 0
	global_load_lds_dwordx4 v[182:183], off
	v_lshl_add_u64 v[182:183], v[176:177], 0, s[16:17]
	s_mov_b32 m0, s47
	s_nop 0
	global_load_lds_dwordx4 v[182:183], off
	v_lshl_add_u64 v[182:183], v[178:179], 0, s[16:17]
	s_mov_b32 m0, s50
	s_nop 0
	global_load_lds_dwordx4 v[182:183], off
	s_add_i32 s2, s67, 0x10000
	v_add3_u32 v180, s2, v221, v0
	ds_read_b128 v[182:185], v180
	s_waitcnt lgkmcnt(0)
	v_mfma_f32_32x32x16_bf16 v[2:17], v[158:161], v[182:185], v[2:17]
	ds_read_b128 v[182:185], v180 offset:8192
	s_waitcnt lgkmcnt(0)
	v_mfma_f32_32x32x16_bf16 v[18:33], v[158:161], v[182:185], v[18:33]
	ds_read_b128 v[182:185], v180 offset:16384
	s_waitcnt lgkmcnt(0)
	v_mfma_f32_32x32x16_bf16 v[34:49], v[158:161], v[182:185], v[34:49]
	ds_read_b128 v[182:185], v180 offset:24576
	s_waitcnt lgkmcnt(0)
	v_mfma_f32_32x32x16_bf16 v[50:65], v[158:161], v[182:185], v[50:65]
	v_bitop3_b32 v158, v215, v210, 15 bitop3:0x78
	v_lshlrev_b32_e32 v159, 4, v158
	v_add3_u32 v158, s2, v159, v0
	ds_read_b128 v[182:185], v158
	s_waitcnt lgkmcnt(0)
	v_mfma_f32_32x32x16_bf16 v[2:17], v[154:157], v[182:185], v[2:17]
	ds_read_b128 v[182:185], v158 offset:8192
	s_waitcnt lgkmcnt(0)
	v_mfma_f32_32x32x16_bf16 v[18:33], v[154:157], v[182:185], v[18:33]
	ds_read_b128 v[182:185], v158 offset:16384
	s_waitcnt lgkmcnt(0)
	v_mfma_f32_32x32x16_bf16 v[34:49], v[154:157], v[182:185], v[34:49]
	ds_read_b128 v[182:185], v158 offset:24576
	s_waitcnt lgkmcnt(0)
	v_mfma_f32_32x32x16_bf16 v[50:65], v[154:157], v[182:185], v[50:65]
	v_bitop3_b32 v154, v216, v210, 15 bitop3:0x78
	v_lshlrev_b32_e32 v155, 4, v154
	v_add3_u32 v154, s2, v155, v0
	ds_read_b128 v[182:185], v154
	s_waitcnt lgkmcnt(0)
	v_mfma_f32_32x32x16_bf16 v[2:17], v[150:153], v[182:185], v[2:17]
	ds_read_b128 v[182:185], v154 offset:8192
	s_waitcnt lgkmcnt(0)
	v_mfma_f32_32x32x16_bf16 v[18:33], v[150:153], v[182:185], v[18:33]
	ds_read_b128 v[182:185], v154 offset:16384
	s_waitcnt lgkmcnt(0)
	v_mfma_f32_32x32x16_bf16 v[34:49], v[150:153], v[182:185], v[34:49]
	ds_read_b128 v[182:185], v154 offset:24576
	s_waitcnt lgkmcnt(0)
	v_mfma_f32_32x32x16_bf16 v[50:65], v[150:153], v[182:185], v[50:65]
	v_bitop3_b32 v150, v217, v210, 15 bitop3:0x78
	v_lshlrev_b32_e32 v151, 4, v150
	v_add3_u32 v150, s2, v151, v0
	ds_read_b128 v[182:185], v150
	s_waitcnt lgkmcnt(0)
	v_mfma_f32_32x32x16_bf16 v[2:17], v[146:149], v[182:185], v[2:17]
	ds_read_b128 v[182:185], v150 offset:8192
	s_waitcnt lgkmcnt(0)
	v_mfma_f32_32x32x16_bf16 v[18:33], v[146:149], v[182:185], v[18:33]
	ds_read_b128 v[182:185], v150 offset:16384
	s_waitcnt lgkmcnt(0)
	v_mfma_f32_32x32x16_bf16 v[34:49], v[146:149], v[182:185], v[34:49]
	ds_read_b128 v[182:185], v150 offset:24576
	s_waitcnt lgkmcnt(0)
	v_mfma_f32_32x32x16_bf16 v[50:65], v[146:149], v[182:185], v[50:65]
	v_bitop3_b32 v146, v218, v210, 15 bitop3:0x78
	v_lshlrev_b32_e32 v147, 4, v146
	v_add3_u32 v146, s2, v147, v0
	ds_read_b128 v[182:185], v146
	s_waitcnt lgkmcnt(0)
	v_mfma_f32_32x32x16_bf16 v[2:17], v[142:145], v[182:185], v[2:17]
	ds_read_b128 v[182:185], v146 offset:8192
	s_waitcnt lgkmcnt(0)
	v_mfma_f32_32x32x16_bf16 v[18:33], v[142:145], v[182:185], v[18:33]
	ds_read_b128 v[182:185], v146 offset:16384
	s_waitcnt lgkmcnt(0)
	v_mfma_f32_32x32x16_bf16 v[34:49], v[142:145], v[182:185], v[34:49]
	ds_read_b128 v[182:185], v146 offset:24576
	s_waitcnt lgkmcnt(0)
	v_mfma_f32_32x32x16_bf16 v[50:65], v[142:145], v[182:185], v[50:65]
	v_bitop3_b32 v142, v219, v210, 15 bitop3:0x78
	v_lshlrev_b32_e32 v145, 4, v142
	v_add3_u32 v142, s2, v145, v0
	ds_read_b128 v[182:185], v142
	s_waitcnt lgkmcnt(0)
; #define RM_WAITBAR() asm volatile("s_waitcnt vmcnt(0) lgkmcnt(0)\n\ts_barrier" ::: "memory")
; #define RM_DMA_V(p, buf) do { _Pragma("unroll") for (int i = 0; i < 8; ++i) { const int idx = tid + 512 * i, tok = (idx >> 2) & 127; \
;         glds16(PROJ + (size_t)2 * T * 1024 + (hb0 + tok) * 512 + (p) * 256 + (idx >> 9) * 32 + (idx & 3) * 8, (unsigned)__builtin_amdgcn_readfirstlane(ldsb + (buf) * 65536 + i * 8192)); } } while (0)
; #define RM_DMA_ST(p, dkh, buf) do { _Pragma("unroll") for (int i = 0; i < 8; ++i) { const int idx = tid + 512 * i, e = idx >> 4, c = (idx & 15) ^ (e & 15); \
;         glds16(stb + (size_t)((p) * 256 + e) * 256 + (dkh) * 128 + c * 8, (unsigned)__builtin_amdgcn_readfirstlane(ldsb + (buf) * 65536 + i * 8192)); } } while (0)
; #define RM_QA(DKH) do { _Pragma("unroll") for (int sl = 0; sl < 8; ++sl) qa[sl] = *(const GAS bf16x8*)(qrow + 16 * ((DKH) * 8 + sl)); } while (0)
; #define RM_QA_USE() asm volatile("" :: "v"(qa[0]), "v"(qa[1]), "v"(qa[2]), "v"(qa[3]), "v"(qa[4]), "v"(qa[5]), "v"(qa[6]), "v"(qa[7]))
; __device__ __forceinline__ void ret_main_phase(Frame& F, const bf16* PROJ, const bf16* ST, bf16* AO) { LTID();
;     ...
;         bf16x8 qa[8];
;         RM_WAITBAR(); RM_DMA_V(1, 0);      RM_PV(1, 0);
;         RM_WAITBAR(); RM_DMA_ST(0, 0, 1);  RM_PV(0, 4);
;         RM_QA(0); RM_WAITBAR(); RM_QA_USE(); RM_DMA_ST(0, 1, 0);  RM_CROSS(1, 0);
;         RM_QA(1); RM_WAITBAR(); RM_QA_USE(); RM_DMA_ST(1, 0, 1);  RM_CROSS(0, 0);
;         RM_QA(0); RM_WAITBAR(); RM_QA_USE(); RM_DMA_ST(1, 1, 0);  RM_CROSS(1, 4);
	v_mfma_f32_32x32x16_bf16 v[2:17], v[138:141], v[182:185], v[2:17]
	ds_read_b128 v[182:185], v142 offset:8192
	s_waitcnt lgkmcnt(0)
	v_mfma_f32_32x32x16_bf16 v[18:33], v[138:141], v[182:185], v[18:33]
	ds_read_b128 v[182:185], v142 offset:16384
	s_waitcnt lgkmcnt(0)
	v_mfma_f32_32x32x16_bf16 v[34:49], v[138:141], v[182:185], v[34:49]
	ds_read_b128 v[182:185], v142 offset:24576
	s_waitcnt lgkmcnt(0)
	v_mfma_f32_32x32x16_bf16 v[50:65], v[138:141], v[182:185], v[50:65]
	v_bitop3_b32 v138, v220, v210, 15 bitop3:0x78
	v_lshlrev_b32_e32 v152, 4, v138
	v_add3_u32 v143, s2, v152, v0
	ds_read_b128 v[138:141], v143
	s_waitcnt lgkmcnt(0)
	v_mfma_f32_32x32x16_bf16 v[2:17], v[134:137], v[138:141], v[2:17]
	ds_read_b128 v[138:141], v143 offset:8192
	s_waitcnt lgkmcnt(0)
	v_mfma_f32_32x32x16_bf16 v[18:33], v[134:137], v[138:141], v[18:33]
	ds_read_b128 v[138:141], v143 offset:16384
	s_waitcnt lgkmcnt(0)
	v_mfma_f32_32x32x16_bf16 v[34:49], v[134:137], v[138:141], v[34:49]
	ds_read_b128 v[138:141], v143 offset:24576
	s_waitcnt lgkmcnt(0)
	v_mfma_f32_32x32x16_bf16 v[50:65], v[134:137], v[138:141], v[50:65]
	v_bitop3_b32 v134, v181, v210, 15 bitop3:0x78
	v_lshlrev_b32_e32 v153, 4, v134
	v_add3_u32 v144, s2, v153, v0
	ds_read_b128 v[134:137], v144
	s_waitcnt lgkmcnt(0)
	v_mfma_f32_32x32x16_bf16 v[2:17], v[130:133], v[134:137], v[2:17]
	ds_read_b128 v[134:137], v144 offset:8192
	s_waitcnt lgkmcnt(0)
	v_mfma_f32_32x32x16_bf16 v[18:33], v[130:133], v[134:137], v[18:33]
	ds_read_b128 v[134:137], v144 offset:16384
	s_waitcnt lgkmcnt(0)
	v_mfma_f32_32x32x16_bf16 v[34:49], v[130:133], v[134:137], v[34:49]
	ds_read_b128 v[134:137], v144 offset:24576
	s_waitcnt lgkmcnt(0)
	v_mfma_f32_32x32x16_bf16 v[50:65], v[130:133], v[134:137], v[50:65]
	global_load_dwordx4 v[182:185], v[162:163], off offset:256
	global_load_dwordx4 v[186:189], v[162:163], off offset:288
	global_load_dwordx4 v[190:193], v[162:163], off offset:320
	global_load_dwordx4 v[194:197], v[162:163], off offset:352
	global_load_dwordx4 v[198:201], v[162:163], off offset:384
	global_load_dwordx4 v[138:141], v[162:163], off offset:416
	global_load_dwordx4 v[134:137], v[162:163], off offset:448
	global_load_dwordx4 v[130:133], v[162:163], off offset:480
	s_waitcnt vmcnt(0) lgkmcnt(0)
	s_barrier
	v_lshl_add_u64 v[148:149], v[164:165], 0, s[76:77]
	v_add3_u32 v181, s67, v221, v0
	s_waitcnt vmcnt(0)
	s_mov_b32 m0, s0
	s_nop 0
	global_load_lds_dwordx4 v[148:149], off
	v_lshl_add_u64 v[148:149], v[166:167], 0, s[76:77]
	s_mov_b32 m0, s43
	s_nop 0
	global_load_lds_dwordx4 v[148:149], off
	v_lshl_add_u64 v[148:149], v[168:169], 0, s[76:77]
	s_mov_b32 m0, s44
	s_nop 0
	global_load_lds_dwordx4 v[148:149], off
	v_lshl_add_u64 v[148:149], v[170:171], 0, s[76:77]
	s_mov_b32 m0, s45
	s_nop 0
	global_load_lds_dwordx4 v[148:149], off
	v_lshl_add_u64 v[148:149], v[172:173], 0, s[76:77]
	s_mov_b32 m0, s51
	s_nop 0
	global_load_lds_dwordx4 v[148:149], off
	v_lshl_add_u64 v[148:149], v[174:175], 0, s[76:77]
	s_mov_b32 m0, s56
	s_nop 0
	global_load_lds_dwordx4 v[148:149], off
	v_lshl_add_u64 v[148:149], v[176:177], 0, s[76:77]
	s_mov_b32 m0, s62
	s_nop 0
	global_load_lds_dwordx4 v[148:149], off
	v_lshl_add_u64 v[148:149], v[178:179], 0, s[76:77]
	s_mov_b32 m0, s63
	s_nop 0
	global_load_lds_dwordx4 v[148:149], off
	ds_read_b128 v[216:219], v181
	s_waitcnt lgkmcnt(0)
	v_mfma_f32_32x32x16_bf16 v[2:17], v[182:185], v[216:219], v[2:17]
	ds_read_b128 v[216:219], v181 offset:8192
	s_waitcnt lgkmcnt(0)
	v_mfma_f32_32x32x16_bf16 v[18:33], v[182:185], v[216:219], v[18:33]
	ds_read_b128 v[216:219], v181 offset:16384
	s_waitcnt lgkmcnt(0)
	v_mfma_f32_32x32x16_bf16 v[34:49], v[182:185], v[216:219], v[34:49]
	ds_read_b128 v[216:219], v181 offset:24576
	s_waitcnt lgkmcnt(0)
	v_mfma_f32_32x32x16_bf16 v[50:65], v[182:185], v[216:219], v[50:65]
	v_add3_u32 v215, s67, v159, v0
	ds_read_b128 v[182:185], v215
	s_waitcnt lgkmcnt(0)
	v_mfma_f32_32x32x16_bf16 v[2:17], v[186:189], v[182:185], v[2:17]
	ds_read_b128 v[182:185], v215 offset:8192
	s_waitcnt lgkmcnt(0)
	v_mfma_f32_32x32x16_bf16 v[18:33], v[186:189], v[182:185], v[18:33]
	ds_read_b128 v[182:185], v215 offset:16384
	s_waitcnt lgkmcnt(0)
	v_mfma_f32_32x32x16_bf16 v[34:49], v[186:189], v[182:185], v[34:49]
	ds_read_b128 v[182:185], v215 offset:24576
	s_waitcnt lgkmcnt(0)
	v_mfma_f32_32x32x16_bf16 v[50:65], v[186:189], v[182:185], v[50:65]
	v_add3_u32 v216, s67, v155, v0
	ds_read_b128 v[182:185], v216
	s_waitcnt lgkmcnt(0)
	v_mfma_f32_32x32x16_bf16 v[2:17], v[190:193], v[182:185], v[2:17]
	ds_read_b128 v[182:185], v216 offset:8192
	s_waitcnt lgkmcnt(0)
	v_mfma_f32_32x32x16_bf16 v[18:33], v[190:193], v[182:185], v[18:33]
	ds_read_b128 v[182:185], v216 offset:16384
	s_waitcnt lgkmcnt(0)
	v_mfma_f32_32x32x16_bf16 v[34:49], v[190:193], v[182:185], v[34:49]
	ds_read_b128 v[182:185], v216 offset:24576
	s_waitcnt lgkmcnt(0)
	v_mfma_f32_32x32x16_bf16 v[50:65], v[190:193], v[182:185], v[50:65]
	v_add3_u32 v217, s67, v151, v0
	ds_read_b128 v[182:185], v217
	s_waitcnt lgkmcnt(0)
	v_mfma_f32_32x32x16_bf16 v[2:17], v[194:197], v[182:185], v[2:17]
	ds_read_b128 v[182:185], v217 offset:8192
	s_waitcnt lgkmcnt(0)
	v_mfma_f32_32x32x16_bf16 v[18:33], v[194:197], v[182:185], v[18:33]
	ds_read_b128 v[182:185], v217 offset:16384
	s_waitcnt lgkmcnt(0)
	v_mfma_f32_32x32x16_bf16 v[34:49], v[194:197], v[182:185], v[34:49]
	ds_read_b128 v[182:185], v217 offset:24576
	s_waitcnt lgkmcnt(0)
	v_mfma_f32_32x32x16_bf16 v[50:65], v[194:197], v[182:185], v[50:65]
	v_add3_u32 v218, s67, v147, v0
	ds_read_b128 v[182:185], v218
	s_waitcnt lgkmcnt(0)
	v_mfma_f32_32x32x16_bf16 v[2:17], v[198:201], v[182:185], v[2:17]
	ds_read_b128 v[182:185], v218 offset:8192
	s_waitcnt lgkmcnt(0)
; #define RM_WAITBAR() asm volatile("s_waitcnt vmcnt(0) lgkmcnt(0)\n\ts_barrier" ::: "memory")
; #define RM_DMA_V(p, buf) do { _Pragma("unroll") for (int i = 0; i < 8; ++i) { const int idx = tid + 512 * i, tok = (idx >> 2) & 127; \
;         glds16(PROJ + (size_t)2 * T * 1024 + (hb0 + tok) * 512 + (p) * 256 + (idx >> 9) * 32 + (idx & 3) * 8, (unsigned)__builtin_amdgcn_readfirstlane(ldsb + (buf) * 65536 + i * 8192)); } } while (0)
; #define RM_DMA_ST(p, dkh, buf) do { _Pragma("unroll") for (int i = 0; i < 8; ++i) { const int idx = tid + 512 * i, e = idx >> 4, c = (idx & 15) ^ (e & 15); \
;         glds16(stb + (size_t)((p) * 256 + e) * 256 + (dkh) * 128 + c * 8, (unsigned)__builtin_amdgcn_readfirstlane(ldsb + (buf) * 65536 + i * 8192)); } } while (0)
; #define RM_QA(DKH) do { _Pragma("unroll") for (int sl = 0; sl < 8; ++sl) qa[sl] = *(const GAS bf16x8*)(qrow + 16 * ((DKH) * 8 + sl)); } while (0)
; #define RM_QA_USE() asm volatile("" :: "v"(qa[0]), "v"(qa[1]), "v"(qa[2]), "v"(qa[3]), "v"(qa[4]), "v"(qa[5]), "v"(qa[6]), "v"(qa[7]))
; __device__ __forceinline__ void ret_main_phase(Frame& F, const bf16* PROJ, const bf16* ST, bf16* AO) { LTID();
;     ...
;         bf16x8 qa[8];
;         RM_WAITBAR(); RM_DMA_V(1, 0);      RM_PV(1, 0);
;         RM_WAITBAR(); RM_DMA_ST(0, 0, 1);  RM_PV(0, 4);
;         RM_QA(0); RM_WAITBAR(); RM_QA_USE(); RM_DMA_ST(0, 1, 0);  RM_CROSS(1, 0);
;         RM_QA(1); RM_WAITBAR(); RM_QA_USE(); RM_DMA_ST(1, 0, 1);  RM_CROSS(0, 0);
;         RM_QA(0); RM_WAITBAR(); RM_QA_USE(); RM_DMA_ST(1, 1, 0);  RM_CROSS(1, 4);
	v_mfma_f32_32x32x16_bf16 v[18:33], v[198:201], v[182:185], v[18:33]
	ds_read_b128 v[182:185], v218 offset:16384
	s_waitcnt lgkmcnt(0)
	v_mfma_f32_32x32x16_bf16 v[34:49], v[198:201], v[182:185], v[34:49]
	ds_read_b128 v[182:185], v218 offset:24576
	s_waitcnt lgkmcnt(0)
	v_mfma_f32_32x32x16_bf16 v[50:65], v[198:201], v[182:185], v[50:65]
	v_add3_u32 v219, s67, v145, v0
	ds_read_b128 v[182:185], v219
	s_waitcnt lgkmcnt(0)
	v_mfma_f32_32x32x16_bf16 v[2:17], v[138:141], v[182:185], v[2:17]
	ds_read_b128 v[182:185], v219 offset:8192
	s_waitcnt lgkmcnt(0)
	v_mfma_f32_32x32x16_bf16 v[18:33], v[138:141], v[182:185], v[18:33]
	ds_read_b128 v[182:185], v219 offset:16384
	s_waitcnt lgkmcnt(0)
	v_mfma_f32_32x32x16_bf16 v[34:49], v[138:141], v[182:185], v[34:49]
	ds_read_b128 v[182:185], v219 offset:24576
	s_waitcnt lgkmcnt(0)
	v_mfma_f32_32x32x16_bf16 v[50:65], v[138:141], v[182:185], v[50:65]
	v_add3_u32 v220, s67, v152, v0
	ds_read_b128 v[138:141], v220
	s_waitcnt lgkmcnt(0)
	v_mfma_f32_32x32x16_bf16 v[2:17], v[134:137], v[138:141], v[2:17]
	ds_read_b128 v[138:141], v220 offset:8192
	s_waitcnt lgkmcnt(0)
	v_mfma_f32_32x32x16_bf16 v[18:33], v[134:137], v[138:141], v[18:33]
	ds_read_b128 v[138:141], v220 offset:16384
	s_waitcnt lgkmcnt(0)
	v_mfma_f32_32x32x16_bf16 v[34:49], v[134:137], v[138:141], v[34:49]
	ds_read_b128 v[138:141], v220 offset:24576
	s_waitcnt lgkmcnt(0)
	v_mfma_f32_32x32x16_bf16 v[50:65], v[134:137], v[138:141], v[50:65]
	v_add3_u32 v0, s67, v153, v0
	ds_read_b128 v[134:137], v0
	s_waitcnt lgkmcnt(0)
	v_mfma_f32_32x32x16_bf16 v[2:17], v[130:133], v[134:137], v[2:17]
	ds_read_b128 v[134:137], v0 offset:8192
	s_waitcnt lgkmcnt(0)
	v_mfma_f32_32x32x16_bf16 v[18:33], v[130:133], v[134:137], v[18:33]
	ds_read_b128 v[134:137], v0 offset:16384
	s_waitcnt lgkmcnt(0)
	v_mfma_f32_32x32x16_bf16 v[34:49], v[130:133], v[134:137], v[34:49]
	ds_read_b128 v[134:137], v0 offset:24576
	s_waitcnt lgkmcnt(0)
	v_mfma_f32_32x32x16_bf16 v[50:65], v[130:133], v[134:137], v[50:65]
	global_load_dwordx4 v[130:133], v[162:163], off
	global_load_dwordx4 v[134:137], v[162:163], off offset:32
	global_load_dwordx4 v[138:141], v[162:163], off offset:64
	global_load_dwordx4 v[182:185], v[162:163], off offset:96
	global_load_dwordx4 v[186:189], v[162:163], off offset:128
	global_load_dwordx4 v[190:193], v[162:163], off offset:160
	global_load_dwordx4 v[194:197], v[162:163], off offset:192
	global_load_dwordx4 v[198:201], v[162:163], off offset:224
	s_waitcnt vmcnt(0) lgkmcnt(0)
	s_barrier
	v_lshl_add_u64 v[148:149], v[164:165], 0, s[84:85]
	v_lshl_add_u64 v[152:153], v[166:167], 0, s[84:85]
	v_lshl_add_u64 v[156:157], v[168:169], 0, s[84:85]
	v_lshl_add_u64 v[160:161], v[170:171], 0, s[84:85]
	v_lshl_add_u64 v[164:165], v[172:173], 0, s[84:85]
	v_lshl_add_u64 v[166:167], v[174:175], 0, s[84:85]
	v_lshl_add_u64 v[168:169], v[176:177], 0, s[84:85]
	v_lshl_add_u64 v[170:171], v[178:179], 0, s[84:85]
	s_waitcnt vmcnt(0)
	s_mov_b32 m0, s65
	s_nop 0
	global_load_lds_dwordx4 v[148:149], off
	s_nop 0
	s_mov_b32 m0, s68
	s_nop 0
	global_load_lds_dwordx4 v[152:153], off
	s_nop 0
	s_mov_b32 m0, s69
	s_nop 0
	global_load_lds_dwordx4 v[156:157], off
	s_nop 0
	s_mov_b32 m0, s70
	s_nop 0
	global_load_lds_dwordx4 v[160:161], off
	s_nop 0
	s_mov_b32 m0, s46
	s_nop 0
	global_load_lds_dwordx4 v[164:165], off
	s_nop 0
	s_mov_b32 m0, s42
	s_nop 0
	global_load_lds_dwordx4 v[166:167], off
	s_nop 0
	s_mov_b32 m0, s47
	s_nop 0
	global_load_lds_dwordx4 v[168:169], off
	s_nop 0
	s_mov_b32 m0, s50
	s_nop 0
	global_load_lds_dwordx4 v[170:171], off
	ds_read_b128 v[164:167], v180
	ds_read_b128 v[168:171], v180 offset:8192
	s_waitcnt lgkmcnt(1)
	v_mfma_f32_32x32x16_bf16 v[66:81], v[130:133], v[164:167], v[66:81]
	s_waitcnt lgkmcnt(0)
	v_mfma_f32_32x32x16_bf16 v[82:97], v[130:133], v[168:171], v[82:97]
	ds_read_b128 v[164:167], v180 offset:16384
	ds_read_b128 v[168:171], v180 offset:24576
	s_waitcnt lgkmcnt(1)
	v_mfma_f32_32x32x16_bf16 v[98:113], v[130:133], v[164:167], v[98:113]
	s_waitcnt lgkmcnt(0)
	v_mfma_f32_32x32x16_bf16 v[114:129], v[130:133], v[168:171], v[114:129]
	ds_read_b128 v[130:133], v158
	s_waitcnt lgkmcnt(0)
	v_mfma_f32_32x32x16_bf16 v[66:81], v[134:137], v[130:133], v[66:81]
	ds_read_b128 v[130:133], v158 offset:8192
	s_waitcnt lgkmcnt(0)
	v_mfma_f32_32x32x16_bf16 v[82:97], v[134:137], v[130:133], v[82:97]
	ds_read_b128 v[130:133], v158 offset:16384
	s_waitcnt lgkmcnt(0)
	v_mfma_f32_32x32x16_bf16 v[98:113], v[134:137], v[130:133], v[98:113]
	ds_read_b128 v[130:133], v158 offset:24576
	s_waitcnt lgkmcnt(0)
	v_mfma_f32_32x32x16_bf16 v[114:129], v[134:137], v[130:133], v[114:129]
	ds_read_b128 v[130:133], v154
	s_waitcnt lgkmcnt(0)
	v_mfma_f32_32x32x16_bf16 v[66:81], v[138:141], v[130:133], v[66:81]
	ds_read_b128 v[130:133], v154 offset:8192
	s_waitcnt lgkmcnt(0)
	v_mfma_f32_32x32x16_bf16 v[82:97], v[138:141], v[130:133], v[82:97]
	ds_read_b128 v[130:133], v154 offset:16384
	s_waitcnt lgkmcnt(0)
	v_mfma_f32_32x32x16_bf16 v[98:113], v[138:141], v[130:133], v[98:113]
	ds_read_b128 v[130:133], v154 offset:24576
	s_waitcnt lgkmcnt(0)
	v_mfma_f32_32x32x16_bf16 v[114:129], v[138:141], v[130:133], v[114:129]
	ds_read_b128 v[130:133], v150
	s_waitcnt lgkmcnt(0)
	v_mfma_f32_32x32x16_bf16 v[66:81], v[182:185], v[130:133], v[66:81]
	ds_read_b128 v[130:133], v150 offset:8192
	s_waitcnt lgkmcnt(0)
	v_mfma_f32_32x32x16_bf16 v[82:97], v[182:185], v[130:133], v[82:97]
	ds_read_b128 v[130:133], v150 offset:16384
	s_waitcnt lgkmcnt(0)
	v_mfma_f32_32x32x16_bf16 v[98:113], v[182:185], v[130:133], v[98:113]
	ds_read_b128 v[130:133], v150 offset:24576
	s_waitcnt lgkmcnt(0)
; #define RM_WAITBAR() asm volatile("s_waitcnt vmcnt(0) lgkmcnt(0)\n\ts_barrier" ::: "memory")
; #define RM_DMA_V(p, buf) do { _Pragma("unroll") for (int i = 0; i < 8; ++i) { const int idx = tid + 512 * i, tok = (idx >> 2) & 127; \
;         glds16(PROJ + (size_t)2 * T * 1024 + (hb0 + tok) * 512 + (p) * 256 + (idx >> 9) * 32 + (idx & 3) * 8, (unsigned)__builtin_amdgcn_readfirstlane(ldsb + (buf) * 65536 + i * 8192)); } } while (0)
; #define RM_DMA_ST(p, dkh, buf) do { _Pragma("unroll") for (int i = 0; i < 8; ++i) { const int idx = tid + 512 * i, e = idx >> 4, c = (idx & 15) ^ (e & 15); \
;         glds16(stb + (size_t)((p) * 256 + e) * 256 + (dkh) * 128 + c * 8, (unsigned)__builtin_amdgcn_readfirstlane(ldsb + (buf) * 65536 + i * 8192)); } } while (0)
; #define RM_QA(DKH) do { _Pragma("unroll") for (int sl = 0; sl < 8; ++sl) qa[sl] = *(const GAS bf16x8*)(qrow + 16 * ((DKH) * 8 + sl)); } while (0)
; #define RM_QA_USE() asm volatile("" :: "v"(qa[0]), "v"(qa[1]), "v"(qa[2]), "v"(qa[3]), "v"(qa[4]), "v"(qa[5]), "v"(qa[6]), "v"(qa[7]))
; __device__ __forceinline__ void ret_main_phase(Frame& F, const bf16* PROJ, const bf16* ST, bf16* AO) { LTID();
;     ...
;         bf16x8 qa[8];
;         RM_WAITBAR(); RM_DMA_V(1, 0);      RM_PV(1, 0);
;         RM_WAITBAR(); RM_DMA_ST(0, 0, 1);  RM_PV(0, 4);
;         RM_QA(0); RM_WAITBAR(); RM_QA_USE(); RM_DMA_ST(0, 1, 0);  RM_CROSS(1, 0);
;         RM_QA(1); RM_WAITBAR(); RM_QA_USE(); RM_DMA_ST(1, 0, 1);  RM_CROSS(0, 0);
;         RM_QA(0); RM_WAITBAR(); RM_QA_USE(); RM_DMA_ST(1, 1, 0);  RM_CROSS(1, 4);
;         RM_QA(1); RM_WAITBAR(); RM_QA_USE();                      RM_CROSS(0, 4);
	v_mfma_f32_32x32x16_bf16 v[114:129], v[182:185], v[130:133], v[114:129]
	ds_read_b128 v[130:133], v146
	s_waitcnt lgkmcnt(0)
	v_mfma_f32_32x32x16_bf16 v[66:81], v[186:189], v[130:133], v[66:81]
	ds_read_b128 v[130:133], v146 offset:8192
	s_waitcnt lgkmcnt(0)
	v_mfma_f32_32x32x16_bf16 v[82:97], v[186:189], v[130:133], v[82:97]
	ds_read_b128 v[130:133], v146 offset:16384
	s_waitcnt lgkmcnt(0)
	v_mfma_f32_32x32x16_bf16 v[98:113], v[186:189], v[130:133], v[98:113]
	ds_read_b128 v[130:133], v146 offset:24576
	s_waitcnt lgkmcnt(0)
	v_mfma_f32_32x32x16_bf16 v[114:129], v[186:189], v[130:133], v[114:129]
	ds_read_b128 v[130:133], v142
	s_waitcnt lgkmcnt(0)
	v_mfma_f32_32x32x16_bf16 v[66:81], v[190:193], v[130:133], v[66:81]
	ds_read_b128 v[130:133], v142 offset:8192
	s_waitcnt lgkmcnt(0)
	v_mfma_f32_32x32x16_bf16 v[82:97], v[190:193], v[130:133], v[82:97]
	ds_read_b128 v[130:133], v142 offset:16384
	s_waitcnt lgkmcnt(0)
	v_mfma_f32_32x32x16_bf16 v[98:113], v[190:193], v[130:133], v[98:113]
	ds_read_b128 v[130:133], v142 offset:24576
	s_waitcnt lgkmcnt(0)
	v_mfma_f32_32x32x16_bf16 v[114:129], v[190:193], v[130:133], v[114:129]
	ds_read_b128 v[130:133], v143
	s_waitcnt lgkmcnt(0)
	v_mfma_f32_32x32x16_bf16 v[66:81], v[194:197], v[130:133], v[66:81]
	ds_read_b128 v[130:133], v143 offset:8192
	s_waitcnt lgkmcnt(0)
	v_mfma_f32_32x32x16_bf16 v[82:97], v[194:197], v[130:133], v[82:97]
	ds_read_b128 v[130:133], v143 offset:16384
	s_waitcnt lgkmcnt(0)
	v_mfma_f32_32x32x16_bf16 v[98:113], v[194:197], v[130:133], v[98:113]
	ds_read_b128 v[130:133], v143 offset:24576
	s_waitcnt lgkmcnt(0)
	v_mfma_f32_32x32x16_bf16 v[114:129], v[194:197], v[130:133], v[114:129]
	ds_read_b128 v[130:133], v144
	s_waitcnt lgkmcnt(0)
	v_mfma_f32_32x32x16_bf16 v[66:81], v[198:201], v[130:133], v[66:81]
	ds_read_b128 v[130:133], v144 offset:8192
	s_waitcnt lgkmcnt(0)
	v_mfma_f32_32x32x16_bf16 v[82:97], v[198:201], v[130:133], v[82:97]
	ds_read_b128 v[130:133], v144 offset:16384
	s_waitcnt lgkmcnt(0)
	v_mfma_f32_32x32x16_bf16 v[98:113], v[198:201], v[130:133], v[98:113]
	ds_read_b128 v[130:133], v144 offset:24576
	s_waitcnt lgkmcnt(0)
	v_mfma_f32_32x32x16_bf16 v[114:129], v[198:201], v[130:133], v[114:129]
	global_load_dwordx4 v[130:133], v[162:163], off offset:256
	global_load_dwordx4 v[134:137], v[162:163], off offset:288
	global_load_dwordx4 v[138:141], v[162:163], off offset:320
	global_load_dwordx4 v[142:145], v[162:163], off offset:352
	global_load_dwordx4 v[146:149], v[162:163], off offset:384
	global_load_dwordx4 v[150:153], v[162:163], off offset:416
	global_load_dwordx4 v[154:157], v[162:163], off offset:448
	global_load_dwordx4 v[158:161], v[162:163], off offset:480
	s_waitcnt vmcnt(0) lgkmcnt(0)
	s_barrier
	s_waitcnt vmcnt(0)
	ds_read_b128 v[162:165], v181
	s_waitcnt lgkmcnt(0)
	v_mfma_f32_32x32x16_bf16 v[66:81], v[130:133], v[162:165], v[66:81]
	ds_read_b128 v[162:165], v181 offset:8192
	s_waitcnt lgkmcnt(0)
	v_mfma_f32_32x32x16_bf16 v[82:97], v[130:133], v[162:165], v[82:97]
	ds_read_b128 v[162:165], v181 offset:16384
	s_waitcnt lgkmcnt(0)
	v_mfma_f32_32x32x16_bf16 v[98:113], v[130:133], v[162:165], v[98:113]
	ds_read_b128 v[162:165], v181 offset:24576
	s_waitcnt lgkmcnt(0)
	v_mfma_f32_32x32x16_bf16 v[114:129], v[130:133], v[162:165], v[114:129]
	ds_read_b128 v[130:133], v215
	s_waitcnt lgkmcnt(0)
	v_mfma_f32_32x32x16_bf16 v[66:81], v[134:137], v[130:133], v[66:81]
	ds_read_b128 v[130:133], v215 offset:8192
	s_waitcnt lgkmcnt(0)
	v_mfma_f32_32x32x16_bf16 v[82:97], v[134:137], v[130:133], v[82:97]
	ds_read_b128 v[130:133], v215 offset:16384
	s_waitcnt lgkmcnt(0)
	v_mfma_f32_32x32x16_bf16 v[98:113], v[134:137], v[130:133], v[98:113]
	ds_read_b128 v[130:133], v215 offset:24576
	s_waitcnt lgkmcnt(0)
	v_mfma_f32_32x32x16_bf16 v[114:129], v[134:137], v[130:133], v[114:129]
	ds_read_b128 v[130:133], v216
	s_waitcnt lgkmcnt(0)
	v_mfma_f32_32x32x16_bf16 v[66:81], v[138:141], v[130:133], v[66:81]
	ds_read_b128 v[130:133], v216 offset:8192
	s_waitcnt lgkmcnt(0)
	v_mfma_f32_32x32x16_bf16 v[82:97], v[138:141], v[130:133], v[82:97]
	ds_read_b128 v[130:133], v216 offset:16384
	s_waitcnt lgkmcnt(0)
	v_mfma_f32_32x32x16_bf16 v[98:113], v[138:141], v[130:133], v[98:113]
	ds_read_b128 v[130:133], v216 offset:24576
	s_waitcnt lgkmcnt(0)
	v_mfma_f32_32x32x16_bf16 v[114:129], v[138:141], v[130:133], v[114:129]
	ds_read_b128 v[130:133], v217
	s_waitcnt lgkmcnt(0)
	v_mfma_f32_32x32x16_bf16 v[66:81], v[142:145], v[130:133], v[66:81]
	ds_read_b128 v[130:133], v217 offset:8192
	s_waitcnt lgkmcnt(0)
	v_mfma_f32_32x32x16_bf16 v[82:97], v[142:145], v[130:133], v[82:97]
	ds_read_b128 v[130:133], v217 offset:16384
	s_waitcnt lgkmcnt(0)
	v_mfma_f32_32x32x16_bf16 v[98:113], v[142:145], v[130:133], v[98:113]
	ds_read_b128 v[130:133], v217 offset:24576
	s_waitcnt lgkmcnt(0)
	v_mfma_f32_32x32x16_bf16 v[114:129], v[142:145], v[130:133], v[114:129]
	ds_read_b128 v[130:133], v218
	s_waitcnt lgkmcnt(0)
	v_mfma_f32_32x32x16_bf16 v[66:81], v[146:149], v[130:133], v[66:81]
	ds_read_b128 v[130:133], v218 offset:8192
	s_waitcnt lgkmcnt(0)
	v_mfma_f32_32x32x16_bf16 v[82:97], v[146:149], v[130:133], v[82:97]
	ds_read_b128 v[130:133], v218 offset:16384
	s_waitcnt lgkmcnt(0)
	v_mfma_f32_32x32x16_bf16 v[98:113], v[146:149], v[130:133], v[98:113]
	ds_read_b128 v[130:133], v218 offset:24576
	s_waitcnt lgkmcnt(0)
	v_mfma_f32_32x32x16_bf16 v[114:129], v[146:149], v[130:133], v[114:129]
	ds_read_b128 v[130:133], v219
	s_waitcnt lgkmcnt(0)
	v_mfma_f32_32x32x16_bf16 v[66:81], v[150:153], v[130:133], v[66:81]
	ds_read_b128 v[130:133], v219 offset:8192
	s_waitcnt lgkmcnt(0)
; __device__ __forceinline__ float half_sum32(float v) { v = row_sum16(v); float a; const float b = swap16_other(v, a); return a + b; }
; __device__ __forceinline__ int crow(int r, int hi) { return (r & 3) + 8 * (r >> 2) + 4 * hi; }
; __device__ __forceinline__ void ret_main_phase(Frame& F, const bf16* PROJ, const bf16* ST, bf16* AO) { LTID();
;     ...
;         for (int i = 0; i < 16; ++i) { float s1 = 0.f, s2 = 0.f;
; #pragma unroll
;             for (int eb = 0; eb < 8; ++eb) { s1 += o[eb][i]; s2 += o[eb][i] * o[eb][i]; }
;             s1 = half_sum32(s1); s2 = half_sum32(s2);
;             if (r32 == 0) { part[(e2 * 128 + rg * 32 + crow(i, hh)) * 2] = s1; part[(e2 * 128 + rg * 32 + crow(i, hh)) * 2 + 1] = s2; } }
	v_mfma_f32_32x32x16_bf16 v[82:97], v[150:153], v[130:133], v[82:97]
	ds_read_b128 v[130:133], v219 offset:16384
	s_waitcnt lgkmcnt(0)
	v_mfma_f32_32x32x16_bf16 v[98:113], v[150:153], v[130:133], v[98:113]
	ds_read_b128 v[130:133], v219 offset:24576
	s_waitcnt lgkmcnt(0)
	v_mfma_f32_32x32x16_bf16 v[114:129], v[150:153], v[130:133], v[114:129]
	ds_read_b128 v[130:133], v220
	s_waitcnt lgkmcnt(0)
	v_mfma_f32_32x32x16_bf16 v[66:81], v[154:157], v[130:133], v[66:81]
	ds_read_b128 v[130:133], v220 offset:8192
	s_waitcnt lgkmcnt(0)
	v_mfma_f32_32x32x16_bf16 v[82:97], v[154:157], v[130:133], v[82:97]
	ds_read_b128 v[130:133], v220 offset:16384
	s_waitcnt lgkmcnt(0)
	v_mfma_f32_32x32x16_bf16 v[98:113], v[154:157], v[130:133], v[98:113]
	ds_read_b128 v[130:133], v220 offset:24576
	s_waitcnt lgkmcnt(0)
	v_mfma_f32_32x32x16_bf16 v[114:129], v[154:157], v[130:133], v[114:129]
	ds_read_b128 v[130:133], v0
	s_waitcnt lgkmcnt(0)
	v_mfma_f32_32x32x16_bf16 v[66:81], v[158:161], v[130:133], v[66:81]
	ds_read_b128 v[130:133], v0 offset:8192
	s_waitcnt lgkmcnt(0)
	v_mfma_f32_32x32x16_bf16 v[82:97], v[158:161], v[130:133], v[82:97]
	ds_read_b128 v[130:133], v0 offset:16384
	s_waitcnt lgkmcnt(0)
	v_mfma_f32_32x32x16_bf16 v[98:113], v[158:161], v[130:133], v[98:113]
	ds_read_b128 v[130:133], v0 offset:24576
	s_waitcnt lgkmcnt(0)
	v_mfma_f32_32x32x16_bf16 v[114:129], v[158:161], v[130:133], v[114:129]
	v_add_f32_e32 v130, 0, v2
	v_mul_f32_e32 v131, v18, v18
	v_add_f32_e32 v130, v130, v18
	v_fmac_f32_e32 v131, v2, v2
	v_add_f32_e32 v130, v130, v34
	v_fmac_f32_e32 v131, v34, v34
	v_add_f32_e32 v130, v130, v50
	v_fmac_f32_e32 v131, v50, v50
	v_add_f32_e32 v130, v130, v66
	v_fmac_f32_e32 v131, v66, v66
	v_add_f32_e32 v130, v130, v82
	v_fmac_f32_e32 v131, v82, v82
	v_add_f32_e32 v130, v130, v98
	v_fmac_f32_e32 v131, v98, v98
	v_add_f32_e32 v130, v130, v114
	v_fmac_f32_e32 v131, v114, v114
	v_lshl_or_b32 v0, s66, 7, v214
	v_add_f32_dpp v130, v130, v130 quad_perm:[1,0,3,2] row_mask:0xf bank_mask:0xf bound_ctrl:1
	v_add_f32_dpp v131, v131, v131 quad_perm:[1,0,3,2] row_mask:0xf bank_mask:0xf bound_ctrl:1
	v_cmp_eq_u32_e32 vcc, 0, v213
	v_add_f32_dpp v130, v130, v130 quad_perm:[2,3,0,1] row_mask:0xf bank_mask:0xf bound_ctrl:1
	v_add_f32_dpp v131, v131, v131 quad_perm:[2,3,0,1] row_mask:0xf bank_mask:0xf bound_ctrl:1
	v_or_b32_e32 v0, s64, v0
	v_add_f32_dpp v130, v130, v130 row_half_mirror row_mask:0xf bank_mask:0xf bound_ctrl:1
	v_add_f32_dpp v131, v131, v131 row_half_mirror row_mask:0xf bank_mask:0xf bound_ctrl:1
	s_nop 0
	v_add_f32_dpp v130, v130, v130 row_mirror row_mask:0xf bank_mask:0xf bound_ctrl:1
	v_add_f32_dpp v131, v131, v131 row_mirror row_mask:0xf bank_mask:0xf bound_ctrl:1
	v_mov_b32_e32 v132, v130
	v_mov_b32_e32 v133, v131
	s_nop 1
	v_permlane16_swap_b32 v132, v130
	s_nop 1
	v_permlane16_swap_b32 v133, v131
	s_and_saveexec_b64 s[6:7], vcc
	v_lshl_add_u32 v134, v0, 3, 0
	v_add_u32_e32 v134, 0x20600, v134
	v_pk_add_f32 v[130:131], v[130:131], v[132:133]
	ds_write_b64 v134, v[130:131]
	s_or_b64 exec, exec, s[6:7]
	v_add_f32_e32 v130, 0, v3
	v_mul_f32_e32 v131, v19, v19
	v_add_f32_e32 v130, v130, v19
	v_fmac_f32_e32 v131, v3, v3
	v_add_f32_e32 v130, v130, v35
	v_fmac_f32_e32 v131, v35, v35
	v_add_f32_e32 v130, v130, v51
	v_fmac_f32_e32 v131, v51, v51
	v_add_f32_e32 v130, v130, v67
	v_fmac_f32_e32 v131, v67, v67
	v_add_f32_e32 v130, v130, v83
	v_fmac_f32_e32 v131, v83, v83
	v_add_f32_e32 v130, v130, v99
	v_fmac_f32_e32 v131, v99, v99
	v_add_f32_e32 v130, v130, v115
	v_fmac_f32_e32 v131, v115, v115
	s_nop 0
	v_add_f32_dpp v130, v130, v130 quad_perm:[1,0,3,2] row_mask:0xf bank_mask:0xf bound_ctrl:1
	v_add_f32_dpp v131, v131, v131 quad_perm:[1,0,3,2] row_mask:0xf bank_mask:0xf bound_ctrl:1
	s_nop 0
	v_add_f32_dpp v130, v130, v130 quad_perm:[2,3,0,1] row_mask:0xf bank_mask:0xf bound_ctrl:1
	v_add_f32_dpp v131, v131, v131 quad_perm:[2,3,0,1] row_mask:0xf bank_mask:0xf bound_ctrl:1
	s_nop 0
	v_add_f32_dpp v130, v130, v130 row_half_mirror row_mask:0xf bank_mask:0xf bound_ctrl:1
	v_add_f32_dpp v131, v131, v131 row_half_mirror row_mask:0xf bank_mask:0xf bound_ctrl:1
	s_nop 0
	v_add_f32_dpp v130, v130, v130 row_mirror row_mask:0xf bank_mask:0xf bound_ctrl:1
	v_add_f32_dpp v131, v131, v131 row_mirror row_mask:0xf bank_mask:0xf bound_ctrl:1
	v_mov_b32_e32 v132, v130
	v_mov_b32_e32 v133, v131
	s_nop 1
	v_permlane16_swap_b32 v130, v132
	s_nop 1
	v_permlane16_swap_b32 v131, v133
	s_and_saveexec_b64 s[6:7], vcc
	s_add_i32 s0, 0, 0x20600
	v_lshl_add_u32 v134, v0, 3, s0
	v_pk_add_f32 v[130:131], v[132:133], v[130:131]
	ds_write_b64 v134, v[130:131] offset:8
	s_or_b64 exec, exec, s[6:7]
	v_add_f32_e32 v130, 0, v4
	v_mul_f32_e32 v131, v20, v20
	v_add_f32_e32 v130, v130, v20
	v_fmac_f32_e32 v131, v4, v4
	v_add_f32_e32 v130, v130, v36
	v_fmac_f32_e32 v131, v36, v36
	v_add_f32_e32 v130, v130, v52
	v_fmac_f32_e32 v131, v52, v52
	v_add_f32_e32 v130, v130, v68
	v_fmac_f32_e32 v131, v68, v68
	v_add_f32_e32 v130, v130, v84
	v_fmac_f32_e32 v131, v84, v84
	v_add_f32_e32 v130, v130, v100
	v_fmac_f32_e32 v131, v100, v100
	v_add_f32_e32 v130, v130, v116
	v_fmac_f32_e32 v131, v116, v116
	s_nop 0
	v_add_f32_dpp v130, v130, v130 quad_perm:[1,0,3,2] row_mask:0xf bank_mask:0xf bound_ctrl:1
	v_add_f32_dpp v131, v131, v131 quad_perm:[1,0,3,2] row_mask:0xf bank_mask:0xf bound_ctrl:1
	s_nop 0
	v_add_f32_dpp v130, v130, v130 quad_perm:[2,3,0,1] row_mask:0xf bank_mask:0xf bound_ctrl:1
	v_add_f32_dpp v131, v131, v131 quad_perm:[2,3,0,1] row_mask:0xf bank_mask:0xf bound_ctrl:1
	s_nop 0
	v_add_f32_dpp v130, v130, v130 row_half_mirror row_mask:0xf bank_mask:0xf bound_ctrl:1
; template <int CTRL> __device__ __forceinline__ float dppf(float v) { return __builtin_bit_cast(float, __builtin_amdgcn_update_dpp(0, __builtin_bit_cast(int, v), CTRL, 0xF, 0xF, true)); }
; __device__ __forceinline__ float swap16_other(float v, float& self) { float w; asm volatile("s_nop 1\n\tv_permlane16_swap_b32 %0, %1" : "=v"(w), "+v"(v) : "0"(v)); self = v; return w; }
; __device__ __forceinline__ int crow(int r, int hi) { return (r & 3) + 8 * (r >> 2) + 4 * hi; }
; __device__ __forceinline__ float row_sum16(float v) { v += dppf<0xB1>(v); v += dppf<0x4E>(v); v += dppf<0x141>(v); v += dppf<0x140>(v); return v; }
; __device__ __forceinline__ float row_max16(float v) { v = __builtin_fmaxf(v, dppf<0xB1>(v)); v = __builtin_fmaxf(v, dppf<0x4E>(v)); v = __builtin_fmaxf(v, dppf<0x141>(v)); v = __builtin_fmaxf(v, dppf<0x140>(v)); return v; }
; __device__ __forceinline__ float half_sum32(float v) { v = row_sum16(v); float a; const float b = swap16_other(v, a); return a + b; }
; __device__ __forceinline__ void ret_main_phase(Frame& F, const bf16* PROJ, const bf16* ST, bf16* AO) { LTID();
;     ...
;         for (int i = 0; i < 16; ++i) { float s1 = 0.f, s2 = 0.f;
; #pragma unroll
;             for (int eb = 0; eb < 8; ++eb) { s1 += o[eb][i]; s2 += o[eb][i] * o[eb][i]; }
;             s1 = half_sum32(s1); s2 = half_sum32(s2);
;             if (r32 == 0) { part[(e2 * 128 + rg * 32 + crow(i, hh)) * 2] = s1; part[(e2 * 128 + rg * 32 + crow(i, hh)) * 2 + 1] = s2; } }
	v_add_f32_dpp v131, v131, v131 row_half_mirror row_mask:0xf bank_mask:0xf bound_ctrl:1
	s_nop 0
	v_add_f32_dpp v130, v130, v130 row_mirror row_mask:0xf bank_mask:0xf bound_ctrl:1
	v_add_f32_dpp v131, v131, v131 row_mirror row_mask:0xf bank_mask:0xf bound_ctrl:1
	v_mov_b32_e32 v132, v130
	v_mov_b32_e32 v133, v131
	s_nop 1
	v_permlane16_swap_b32 v130, v132
	s_nop 1
	v_permlane16_swap_b32 v131, v133
	s_and_saveexec_b64 s[6:7], vcc
	s_add_i32 s0, 0, 0x20600
	v_lshl_add_u32 v134, v0, 3, s0
	v_pk_add_f32 v[130:131], v[132:133], v[130:131]
	ds_write_b64 v134, v[130:131] offset:16
	s_or_b64 exec, exec, s[6:7]
	v_add_f32_e32 v130, 0, v5
	v_mul_f32_e32 v131, v21, v21
	v_add_f32_e32 v130, v130, v21
	v_fmac_f32_e32 v131, v5, v5
	v_add_f32_e32 v130, v130, v37
	v_fmac_f32_e32 v131, v37, v37
	v_add_f32_e32 v130, v130, v53
	v_fmac_f32_e32 v131, v53, v53
	v_add_f32_e32 v130, v130, v69
	v_fmac_f32_e32 v131, v69, v69
	v_add_f32_e32 v130, v130, v85
	v_fmac_f32_e32 v131, v85, v85
	v_add_f32_e32 v130, v130, v101
	v_fmac_f32_e32 v131, v101, v101
	v_add_f32_e32 v130, v130, v117
	v_fmac_f32_e32 v131, v117, v117
	s_nop 0
	v_add_f32_dpp v130, v130, v130 quad_perm:[1,0,3,2] row_mask:0xf bank_mask:0xf bound_ctrl:1
	v_add_f32_dpp v131, v131, v131 quad_perm:[1,0,3,2] row_mask:0xf bank_mask:0xf bound_ctrl:1
	s_nop 0
	v_add_f32_dpp v130, v130, v130 quad_perm:[2,3,0,1] row_mask:0xf bank_mask:0xf bound_ctrl:1
	v_add_f32_dpp v131, v131, v131 quad_perm:[2,3,0,1] row_mask:0xf bank_mask:0xf bound_ctrl:1
	s_nop 0
	v_add_f32_dpp v130, v130, v130 row_half_mirror row_mask:0xf bank_mask:0xf bound_ctrl:1
	v_add_f32_dpp v131, v131, v131 row_half_mirror row_mask:0xf bank_mask:0xf bound_ctrl:1
	s_nop 0
	v_add_f32_dpp v130, v130, v130 row_mirror row_mask:0xf bank_mask:0xf bound_ctrl:1
	v_add_f32_dpp v131, v131, v131 row_mirror row_mask:0xf bank_mask:0xf bound_ctrl:1
	v_mov_b32_e32 v132, v130
	v_mov_b32_e32 v133, v131
	s_nop 1
	v_permlane16_swap_b32 v130, v132
	s_nop 1
	v_permlane16_swap_b32 v131, v133
	s_and_saveexec_b64 s[6:7], vcc
	s_add_i32 s0, 0, 0x20600
	v_lshl_add_u32 v134, v0, 3, s0
	v_pk_add_f32 v[130:131], v[132:133], v[130:131]
	ds_write_b64 v134, v[130:131] offset:24
	s_or_b64 exec, exec, s[6:7]
	v_add_f32_e32 v130, 0, v6
	v_mul_f32_e32 v131, v22, v22
	v_add_f32_e32 v130, v130, v22
	v_fmac_f32_e32 v131, v6, v6
	v_add_f32_e32 v130, v130, v38
	v_fmac_f32_e32 v131, v38, v38
	v_add_f32_e32 v130, v130, v54
	v_fmac_f32_e32 v131, v54, v54
	v_add_f32_e32 v130, v130, v70
	v_fmac_f32_e32 v131, v70, v70
	v_add_f32_e32 v130, v130, v86
	v_fmac_f32_e32 v131, v86, v86
	v_add_f32_e32 v130, v130, v102
	v_fmac_f32_e32 v131, v102, v102
	v_add_f32_e32 v130, v130, v118
	v_fmac_f32_e32 v131, v118, v118
	s_nop 0
	v_add_f32_dpp v130, v130, v130 quad_perm:[1,0,3,2] row_mask:0xf bank_mask:0xf bound_ctrl:1
	v_add_f32_dpp v131, v131, v131 quad_perm:[1,0,3,2] row_mask:0xf bank_mask:0xf bound_ctrl:1
	s_nop 0
	v_add_f32_dpp v130, v130, v130 quad_perm:[2,3,0,1] row_mask:0xf bank_mask:0xf bound_ctrl:1
	v_add_f32_dpp v131, v131, v131 quad_perm:[2,3,0,1] row_mask:0xf bank_mask:0xf bound_ctrl:1
	s_nop 0
	v_add_f32_dpp v130, v130, v130 row_half_mirror row_mask:0xf bank_mask:0xf bound_ctrl:1
	v_add_f32_dpp v131, v131, v131 row_half_mirror row_mask:0xf bank_mask:0xf bound_ctrl:1
	s_nop 0
	v_add_f32_dpp v130, v130, v130 row_mirror row_mask:0xf bank_mask:0xf bound_ctrl:1
	v_add_f32_dpp v131, v131, v131 row_mirror row_mask:0xf bank_mask:0xf bound_ctrl:1
	v_mov_b32_e32 v132, v130
	v_mov_b32_e32 v133, v131
	s_nop 1
	v_permlane16_swap_b32 v130, v132
	s_nop 1
	v_permlane16_swap_b32 v131, v133
	s_and_saveexec_b64 s[6:7], vcc
	s_add_i32 s0, 0, 0x20600
	v_lshl_add_u32 v134, v0, 3, s0
	v_pk_add_f32 v[130:131], v[132:133], v[130:131]
	ds_write_b64 v134, v[130:131] offset:64
	s_or_b64 exec, exec, s[6:7]
	v_add_f32_e32 v130, 0, v7
	v_mul_f32_e32 v131, v23, v23
	v_add_f32_e32 v130, v130, v23
	v_fmac_f32_e32 v131, v7, v7
	v_add_f32_e32 v130, v130, v39
	v_fmac_f32_e32 v131, v39, v39
	v_add_f32_e32 v130, v130, v55
	v_fmac_f32_e32 v131, v55, v55
	v_add_f32_e32 v130, v130, v71
	v_fmac_f32_e32 v131, v71, v71
	v_add_f32_e32 v130, v130, v87
	v_fmac_f32_e32 v131, v87, v87
	v_add_f32_e32 v130, v130, v103
	v_fmac_f32_e32 v131, v103, v103
	v_add_f32_e32 v130, v130, v119
	v_fmac_f32_e32 v131, v119, v119
	s_nop 0
	v_add_f32_dpp v130, v130, v130 quad_perm:[1,0,3,2] row_mask:0xf bank_mask:0xf bound_ctrl:1
	v_add_f32_dpp v131, v131, v131 quad_perm:[1,0,3,2] row_mask:0xf bank_mask:0xf bound_ctrl:1
	s_nop 0
	v_add_f32_dpp v130, v130, v130 quad_perm:[2,3,0,1] row_mask:0xf bank_mask:0xf bound_ctrl:1
	v_add_f32_dpp v131, v131, v131 quad_perm:[2,3,0,1] row_mask:0xf bank_mask:0xf bound_ctrl:1
	s_nop 0
	v_add_f32_dpp v130, v130, v130 row_half_mirror row_mask:0xf bank_mask:0xf bound_ctrl:1
	v_add_f32_dpp v131, v131, v131 row_half_mirror row_mask:0xf bank_mask:0xf bound_ctrl:1
	s_nop 0
	v_add_f32_dpp v130, v130, v130 row_mirror row_mask:0xf bank_mask:0xf bound_ctrl:1
	v_add_f32_dpp v131, v131, v131 row_mirror row_mask:0xf bank_mask:0xf bound_ctrl:1
	v_mov_b32_e32 v132, v130
	v_mov_b32_e32 v133, v131
	s_nop 1
	v_permlane16_swap_b32 v130, v132
	s_nop 1
	v_permlane16_swap_b32 v131, v133
	s_and_saveexec_b64 s[6:7], vcc
	s_add_i32 s0, 0, 0x20600
	v_lshl_add_u32 v134, v0, 3, s0
	v_pk_add_f32 v[130:131], v[132:133], v[130:131]
	ds_write_b64 v134, v[130:131] offset:72
	s_or_b64 exec, exec, s[6:7]
	v_add_f32_e32 v130, 0, v8
	v_mul_f32_e32 v131, v24, v24
	v_add_f32_e32 v130, v130, v24
	v_fmac_f32_e32 v131, v8, v8
	v_add_f32_e32 v130, v130, v40
	v_fmac_f32_e32 v131, v40, v40
	v_add_f32_e32 v130, v130, v56
	v_fmac_f32_e32 v131, v56, v56
	v_add_f32_e32 v130, v130, v72
; template <int CTRL> __device__ __forceinline__ float dppf(float v) { return __builtin_bit_cast(float, __builtin_amdgcn_update_dpp(0, __builtin_bit_cast(int, v), CTRL, 0xF, 0xF, true)); }
; __device__ __forceinline__ float swap16_other(float v, float& self) { float w; asm volatile("s_nop 1\n\tv_permlane16_swap_b32 %0, %1" : "=v"(w), "+v"(v) : "0"(v)); self = v; return w; }
; __device__ __forceinline__ int crow(int r, int hi) { return (r & 3) + 8 * (r >> 2) + 4 * hi; }
; __device__ __forceinline__ float row_sum16(float v) { v += dppf<0xB1>(v); v += dppf<0x4E>(v); v += dppf<0x141>(v); v += dppf<0x140>(v); return v; }
; __device__ __forceinline__ float row_max16(float v) { v = __builtin_fmaxf(v, dppf<0xB1>(v)); v = __builtin_fmaxf(v, dppf<0x4E>(v)); v = __builtin_fmaxf(v, dppf<0x141>(v)); v = __builtin_fmaxf(v, dppf<0x140>(v)); return v; }
; __device__ __forceinline__ float half_sum32(float v) { v = row_sum16(v); float a; const float b = swap16_other(v, a); return a + b; }
; __device__ __forceinline__ void ret_main_phase(Frame& F, const bf16* PROJ, const bf16* ST, bf16* AO) { LTID();
;     ...
;         for (int i = 0; i < 16; ++i) { float s1 = 0.f, s2 = 0.f;
; #pragma unroll
;             for (int eb = 0; eb < 8; ++eb) { s1 += o[eb][i]; s2 += o[eb][i] * o[eb][i]; }
;             s1 = half_sum32(s1); s2 = half_sum32(s2);
;             if (r32 == 0) { part[(e2 * 128 + rg * 32 + crow(i, hh)) * 2] = s1; part[(e2 * 128 + rg * 32 + crow(i, hh)) * 2 + 1] = s2; } }
	v_fmac_f32_e32 v131, v72, v72
	v_add_f32_e32 v130, v130, v88
	v_fmac_f32_e32 v131, v88, v88
	v_add_f32_e32 v130, v130, v104
	v_fmac_f32_e32 v131, v104, v104
	v_add_f32_e32 v130, v130, v120
	v_fmac_f32_e32 v131, v120, v120
	s_nop 0
	v_add_f32_dpp v130, v130, v130 quad_perm:[1,0,3,2] row_mask:0xf bank_mask:0xf bound_ctrl:1
	v_add_f32_dpp v131, v131, v131 quad_perm:[1,0,3,2] row_mask:0xf bank_mask:0xf bound_ctrl:1
	s_nop 0
	v_add_f32_dpp v130, v130, v130 quad_perm:[2,3,0,1] row_mask:0xf bank_mask:0xf bound_ctrl:1
	v_add_f32_dpp v131, v131, v131 quad_perm:[2,3,0,1] row_mask:0xf bank_mask:0xf bound_ctrl:1
	s_nop 0
	v_add_f32_dpp v130, v130, v130 row_half_mirror row_mask:0xf bank_mask:0xf bound_ctrl:1
	v_add_f32_dpp v131, v131, v131 row_half_mirror row_mask:0xf bank_mask:0xf bound_ctrl:1
	s_nop 0
	v_add_f32_dpp v130, v130, v130 row_mirror row_mask:0xf bank_mask:0xf bound_ctrl:1
	v_add_f32_dpp v131, v131, v131 row_mirror row_mask:0xf bank_mask:0xf bound_ctrl:1
	v_mov_b32_e32 v132, v130
	v_mov_b32_e32 v133, v131
	s_nop 1
	v_permlane16_swap_b32 v130, v132
	s_nop 1
	v_permlane16_swap_b32 v131, v133
	s_and_saveexec_b64 s[6:7], vcc
	s_add_i32 s0, 0, 0x20600
	v_lshl_add_u32 v134, v0, 3, s0
	v_pk_add_f32 v[130:131], v[132:133], v[130:131]
	ds_write_b64 v134, v[130:131] offset:80
	s_or_b64 exec, exec, s[6:7]
	v_add_f32_e32 v130, 0, v9
	v_mul_f32_e32 v131, v25, v25
	v_add_f32_e32 v130, v130, v25
	v_fmac_f32_e32 v131, v9, v9
	v_add_f32_e32 v130, v130, v41
	v_fmac_f32_e32 v131, v41, v41
	v_add_f32_e32 v130, v130, v57
	v_fmac_f32_e32 v131, v57, v57
	v_add_f32_e32 v130, v130, v73
	v_fmac_f32_e32 v131, v73, v73
	v_add_f32_e32 v130, v130, v89
	v_fmac_f32_e32 v131, v89, v89
	v_add_f32_e32 v130, v130, v105
	v_fmac_f32_e32 v131, v105, v105
	v_add_f32_e32 v130, v130, v121
	v_fmac_f32_e32 v131, v121, v121
	s_nop 0
	v_add_f32_dpp v130, v130, v130 quad_perm:[1,0,3,2] row_mask:0xf bank_mask:0xf bound_ctrl:1
	v_add_f32_dpp v131, v131, v131 quad_perm:[1,0,3,2] row_mask:0xf bank_mask:0xf bound_ctrl:1
	s_nop 0
	v_add_f32_dpp v130, v130, v130 quad_perm:[2,3,0,1] row_mask:0xf bank_mask:0xf bound_ctrl:1
	v_add_f32_dpp v131, v131, v131 quad_perm:[2,3,0,1] row_mask:0xf bank_mask:0xf bound_ctrl:1
	s_nop 0
	v_add_f32_dpp v130, v130, v130 row_half_mirror row_mask:0xf bank_mask:0xf bound_ctrl:1
	v_add_f32_dpp v131, v131, v131 row_half_mirror row_mask:0xf bank_mask:0xf bound_ctrl:1
	s_nop 0
	v_add_f32_dpp v130, v130, v130 row_mirror row_mask:0xf bank_mask:0xf bound_ctrl:1
	v_add_f32_dpp v131, v131, v131 row_mirror row_mask:0xf bank_mask:0xf bound_ctrl:1
	v_mov_b32_e32 v132, v130
	v_mov_b32_e32 v133, v131
	s_nop 1
	v_permlane16_swap_b32 v130, v132
	s_nop 1
	v_permlane16_swap_b32 v131, v133
	s_and_saveexec_b64 s[6:7], vcc
	s_add_i32 s0, 0, 0x20600
	v_lshl_add_u32 v134, v0, 3, s0
	v_pk_add_f32 v[130:131], v[132:133], v[130:131]
	ds_write_b64 v134, v[130:131] offset:88
	s_or_b64 exec, exec, s[6:7]
	v_add_f32_e32 v130, 0, v10
	v_mul_f32_e32 v131, v26, v26
	v_add_f32_e32 v130, v130, v26
	v_fmac_f32_e32 v131, v10, v10
	v_add_f32_e32 v130, v130, v42
	v_fmac_f32_e32 v131, v42, v42
	v_add_f32_e32 v130, v130, v58
	v_fmac_f32_e32 v131, v58, v58
	v_add_f32_e32 v130, v130, v74
	v_fmac_f32_e32 v131, v74, v74
	v_add_f32_e32 v130, v130, v90
	v_fmac_f32_e32 v131, v90, v90
	v_add_f32_e32 v130, v130, v106
	v_fmac_f32_e32 v131, v106, v106
	v_add_f32_e32 v130, v130, v122
	v_fmac_f32_e32 v131, v122, v122
	s_nop 0
	v_add_f32_dpp v130, v130, v130 quad_perm:[1,0,3,2] row_mask:0xf bank_mask:0xf bound_ctrl:1
	v_add_f32_dpp v131, v131, v131 quad_perm:[1,0,3,2] row_mask:0xf bank_mask:0xf bound_ctrl:1
	s_nop 0
	v_add_f32_dpp v130, v130, v130 quad_perm:[2,3,0,1] row_mask:0xf bank_mask:0xf bound_ctrl:1
	v_add_f32_dpp v131, v131, v131 quad_perm:[2,3,0,1] row_mask:0xf bank_mask:0xf bound_ctrl:1
	s_nop 0
	v_add_f32_dpp v130, v130, v130 row_half_mirror row_mask:0xf bank_mask:0xf bound_ctrl:1
	v_add_f32_dpp v131, v131, v131 row_half_mirror row_mask:0xf bank_mask:0xf bound_ctrl:1
	s_nop 0
	v_add_f32_dpp v130, v130, v130 row_mirror row_mask:0xf bank_mask:0xf bound_ctrl:1
	v_add_f32_dpp v131, v131, v131 row_mirror row_mask:0xf bank_mask:0xf bound_ctrl:1
	v_mov_b32_e32 v132, v130
	v_mov_b32_e32 v133, v131
	s_nop 1
	v_permlane16_swap_b32 v130, v132
	s_nop 1
	v_permlane16_swap_b32 v131, v133
	s_and_saveexec_b64 s[6:7], vcc
	s_add_i32 s0, 0, 0x20600
	v_lshl_add_u32 v134, v0, 3, s0
	v_pk_add_f32 v[130:131], v[132:133], v[130:131]
	ds_write_b64 v134, v[130:131] offset:128
	s_or_b64 exec, exec, s[6:7]
	v_add_f32_e32 v130, 0, v11
	v_mul_f32_e32 v131, v27, v27
	v_add_f32_e32 v130, v130, v27
	v_fmac_f32_e32 v131, v11, v11
	v_add_f32_e32 v130, v130, v43
	v_fmac_f32_e32 v131, v43, v43
	v_add_f32_e32 v130, v130, v59
	v_fmac_f32_e32 v131, v59, v59
	v_add_f32_e32 v130, v130, v75
	v_fmac_f32_e32 v131, v75, v75
	v_add_f32_e32 v130, v130, v91
	v_fmac_f32_e32 v131, v91, v91
	v_add_f32_e32 v130, v130, v107
	v_fmac_f32_e32 v131, v107, v107
	v_add_f32_e32 v130, v130, v123
	v_fmac_f32_e32 v131, v123, v123
	s_nop 0
	v_add_f32_dpp v130, v130, v130 quad_perm:[1,0,3,2] row_mask:0xf bank_mask:0xf bound_ctrl:1
	v_add_f32_dpp v131, v131, v131 quad_perm:[1,0,3,2] row_mask:0xf bank_mask:0xf bound_ctrl:1
	s_nop 0
	v_add_f32_dpp v130, v130, v130 quad_perm:[2,3,0,1] row_mask:0xf bank_mask:0xf bound_ctrl:1
	v_add_f32_dpp v131, v131, v131 quad_perm:[2,3,0,1] row_mask:0xf bank_mask:0xf bound_ctrl:1
	s_nop 0
	v_add_f32_dpp v130, v130, v130 row_half_mirror row_mask:0xf bank_mask:0xf bound_ctrl:1
	v_add_f32_dpp v131, v131, v131 row_half_mirror row_mask:0xf bank_mask:0xf bound_ctrl:1
	s_nop 0
	v_add_f32_dpp v130, v130, v130 row_mirror row_mask:0xf bank_mask:0xf bound_ctrl:1
; template <int CTRL> __device__ __forceinline__ float dppf(float v) { return __builtin_bit_cast(float, __builtin_amdgcn_update_dpp(0, __builtin_bit_cast(int, v), CTRL, 0xF, 0xF, true)); }
; __device__ __forceinline__ float swap16_other(float v, float& self) { float w; asm volatile("s_nop 1\n\tv_permlane16_swap_b32 %0, %1" : "=v"(w), "+v"(v) : "0"(v)); self = v; return w; }
; __device__ __forceinline__ int crow(int r, int hi) { return (r & 3) + 8 * (r >> 2) + 4 * hi; }
; __device__ __forceinline__ float row_sum16(float v) { v += dppf<0xB1>(v); v += dppf<0x4E>(v); v += dppf<0x141>(v); v += dppf<0x140>(v); return v; }
; __device__ __forceinline__ float row_max16(float v) { v = __builtin_fmaxf(v, dppf<0xB1>(v)); v = __builtin_fmaxf(v, dppf<0x4E>(v)); v = __builtin_fmaxf(v, dppf<0x141>(v)); v = __builtin_fmaxf(v, dppf<0x140>(v)); return v; }
; __device__ __forceinline__ float half_sum32(float v) { v = row_sum16(v); float a; const float b = swap16_other(v, a); return a + b; }
; __device__ __forceinline__ void ret_main_phase(Frame& F, const bf16* PROJ, const bf16* ST, bf16* AO) { LTID();
;     ...
;         for (int i = 0; i < 16; ++i) { float s1 = 0.f, s2 = 0.f;
; #pragma unroll
;             for (int eb = 0; eb < 8; ++eb) { s1 += o[eb][i]; s2 += o[eb][i] * o[eb][i]; }
;             s1 = half_sum32(s1); s2 = half_sum32(s2);
;             if (r32 == 0) { part[(e2 * 128 + rg * 32 + crow(i, hh)) * 2] = s1; part[(e2 * 128 + rg * 32 + crow(i, hh)) * 2 + 1] = s2; } }
	v_add_f32_dpp v131, v131, v131 row_mirror row_mask:0xf bank_mask:0xf bound_ctrl:1
	v_mov_b32_e32 v132, v130
	v_mov_b32_e32 v133, v131
	s_nop 1
	v_permlane16_swap_b32 v130, v132
	s_nop 1
	v_permlane16_swap_b32 v131, v133
	s_and_saveexec_b64 s[6:7], vcc
	s_add_i32 s0, 0, 0x20600
	v_lshl_add_u32 v134, v0, 3, s0
	v_pk_add_f32 v[130:131], v[132:133], v[130:131]
	ds_write_b64 v134, v[130:131] offset:136
	s_or_b64 exec, exec, s[6:7]
	v_add_f32_e32 v130, 0, v12
	v_mul_f32_e32 v131, v28, v28
	v_add_f32_e32 v130, v130, v28
	v_fmac_f32_e32 v131, v12, v12
	v_add_f32_e32 v130, v130, v44
	v_fmac_f32_e32 v131, v44, v44
	v_add_f32_e32 v130, v130, v60
	v_fmac_f32_e32 v131, v60, v60
	v_add_f32_e32 v130, v130, v76
	v_fmac_f32_e32 v131, v76, v76
	v_add_f32_e32 v130, v130, v92
	v_fmac_f32_e32 v131, v92, v92
	v_add_f32_e32 v130, v130, v108
	v_fmac_f32_e32 v131, v108, v108
	v_add_f32_e32 v130, v130, v124
	v_fmac_f32_e32 v131, v124, v124
	s_nop 0
	v_add_f32_dpp v130, v130, v130 quad_perm:[1,0,3,2] row_mask:0xf bank_mask:0xf bound_ctrl:1
	v_add_f32_dpp v131, v131, v131 quad_perm:[1,0,3,2] row_mask:0xf bank_mask:0xf bound_ctrl:1
	s_nop 0
	v_add_f32_dpp v130, v130, v130 quad_perm:[2,3,0,1] row_mask:0xf bank_mask:0xf bound_ctrl:1
	v_add_f32_dpp v131, v131, v131 quad_perm:[2,3,0,1] row_mask:0xf bank_mask:0xf bound_ctrl:1
	s_nop 0
	v_add_f32_dpp v130, v130, v130 row_half_mirror row_mask:0xf bank_mask:0xf bound_ctrl:1
	v_add_f32_dpp v131, v131, v131 row_half_mirror row_mask:0xf bank_mask:0xf bound_ctrl:1
	s_nop 0
	v_add_f32_dpp v130, v130, v130 row_mirror row_mask:0xf bank_mask:0xf bound_ctrl:1
	v_add_f32_dpp v131, v131, v131 row_mirror row_mask:0xf bank_mask:0xf bound_ctrl:1
	v_mov_b32_e32 v132, v130
	v_mov_b32_e32 v133, v131
	s_nop 1
	v_permlane16_swap_b32 v130, v132
	s_nop 1
	v_permlane16_swap_b32 v131, v133
	s_and_saveexec_b64 s[6:7], vcc
	s_add_i32 s0, 0, 0x20600
	v_lshl_add_u32 v134, v0, 3, s0
	v_pk_add_f32 v[130:131], v[132:133], v[130:131]
	ds_write_b64 v134, v[130:131] offset:144
	s_or_b64 exec, exec, s[6:7]
	v_add_f32_e32 v130, 0, v13
	v_mul_f32_e32 v131, v29, v29
	v_add_f32_e32 v130, v130, v29
	v_fmac_f32_e32 v131, v13, v13
	v_add_f32_e32 v130, v130, v45
	v_fmac_f32_e32 v131, v45, v45
	v_add_f32_e32 v130, v130, v61
	v_fmac_f32_e32 v131, v61, v61
	v_add_f32_e32 v130, v130, v77
	v_fmac_f32_e32 v131, v77, v77
	v_add_f32_e32 v130, v130, v93
	v_fmac_f32_e32 v131, v93, v93
	v_add_f32_e32 v130, v130, v109
	v_fmac_f32_e32 v131, v109, v109
	v_add_f32_e32 v130, v130, v125
	v_fmac_f32_e32 v131, v125, v125
	s_nop 0
	v_add_f32_dpp v130, v130, v130 quad_perm:[1,0,3,2] row_mask:0xf bank_mask:0xf bound_ctrl:1
	v_add_f32_dpp v131, v131, v131 quad_perm:[1,0,3,2] row_mask:0xf bank_mask:0xf bound_ctrl:1
	s_nop 0
	v_add_f32_dpp v130, v130, v130 quad_perm:[2,3,0,1] row_mask:0xf bank_mask:0xf bound_ctrl:1
	v_add_f32_dpp v131, v131, v131 quad_perm:[2,3,0,1] row_mask:0xf bank_mask:0xf bound_ctrl:1
	s_nop 0
	v_add_f32_dpp v130, v130, v130 row_half_mirror row_mask:0xf bank_mask:0xf bound_ctrl:1
	v_add_f32_dpp v131, v131, v131 row_half_mirror row_mask:0xf bank_mask:0xf bound_ctrl:1
	s_nop 0
	v_add_f32_dpp v130, v130, v130 row_mirror row_mask:0xf bank_mask:0xf bound_ctrl:1
	v_add_f32_dpp v131, v131, v131 row_mirror row_mask:0xf bank_mask:0xf bound_ctrl:1
	v_mov_b32_e32 v132, v130
	v_mov_b32_e32 v133, v131
	s_nop 1
	v_permlane16_swap_b32 v130, v132
	s_nop 1
	v_permlane16_swap_b32 v131, v133
	s_and_saveexec_b64 s[6:7], vcc
	s_add_i32 s0, 0, 0x20600
	v_lshl_add_u32 v134, v0, 3, s0
	v_pk_add_f32 v[130:131], v[132:133], v[130:131]
	ds_write_b64 v134, v[130:131] offset:152
	s_or_b64 exec, exec, s[6:7]
	v_add_f32_e32 v130, 0, v14
	v_mul_f32_e32 v131, v30, v30
	v_add_f32_e32 v130, v130, v30
	v_fmac_f32_e32 v131, v14, v14
	v_add_f32_e32 v130, v130, v46
	v_fmac_f32_e32 v131, v46, v46
	v_add_f32_e32 v130, v130, v62
	v_fmac_f32_e32 v131, v62, v62
	v_add_f32_e32 v130, v130, v78
	v_fmac_f32_e32 v131, v78, v78
	v_add_f32_e32 v130, v130, v94
	v_fmac_f32_e32 v131, v94, v94
	v_add_f32_e32 v130, v130, v110
	v_fmac_f32_e32 v131, v110, v110
	v_add_f32_e32 v130, v130, v126
	v_fmac_f32_e32 v131, v126, v126
	s_nop 0
	v_add_f32_dpp v130, v130, v130 quad_perm:[1,0,3,2] row_mask:0xf bank_mask:0xf bound_ctrl:1
	v_add_f32_dpp v131, v131, v131 quad_perm:[1,0,3,2] row_mask:0xf bank_mask:0xf bound_ctrl:1
	s_nop 0
	v_add_f32_dpp v130, v130, v130 quad_perm:[2,3,0,1] row_mask:0xf bank_mask:0xf bound_ctrl:1
	v_add_f32_dpp v131, v131, v131 quad_perm:[2,3,0,1] row_mask:0xf bank_mask:0xf bound_ctrl:1
	s_nop 0
	v_add_f32_dpp v130, v130, v130 row_half_mirror row_mask:0xf bank_mask:0xf bound_ctrl:1
	v_add_f32_dpp v131, v131, v131 row_half_mirror row_mask:0xf bank_mask:0xf bound_ctrl:1
	s_nop 0
	v_add_f32_dpp v130, v130, v130 row_mirror row_mask:0xf bank_mask:0xf bound_ctrl:1
	v_add_f32_dpp v131, v131, v131 row_mirror row_mask:0xf bank_mask:0xf bound_ctrl:1
	v_mov_b32_e32 v132, v130
	v_mov_b32_e32 v133, v131
	s_nop 1
	v_permlane16_swap_b32 v130, v132
	s_nop 1
	v_permlane16_swap_b32 v131, v133
; template <int CTRL> __device__ __forceinline__ float dppf(float v) { return __builtin_bit_cast(float, __builtin_amdgcn_update_dpp(0, __builtin_bit_cast(int, v), CTRL, 0xF, 0xF, true)); }
; __device__ __forceinline__ float swap16_other(float v, float& self) { float w; asm volatile("s_nop 1\n\tv_permlane16_swap_b32 %0, %1" : "=v"(w), "+v"(v) : "0"(v)); self = v; return w; }
; __device__ __forceinline__ int crow(int r, int hi) { return (r & 3) + 8 * (r >> 2) + 4 * hi; }
; __device__ __forceinline__ float row_sum16(float v) { v += dppf<0xB1>(v); v += dppf<0x4E>(v); v += dppf<0x141>(v); v += dppf<0x140>(v); return v; }
; __device__ __forceinline__ float row_max16(float v) { v = __builtin_fmaxf(v, dppf<0xB1>(v)); v = __builtin_fmaxf(v, dppf<0x4E>(v)); v = __builtin_fmaxf(v, dppf<0x141>(v)); v = __builtin_fmaxf(v, dppf<0x140>(v)); return v; }
; __device__ __forceinline__ float half_sum32(float v) { v = row_sum16(v); float a; const float b = swap16_other(v, a); return a + b; }
; __device__ __forceinline__ void ret_main_phase(Frame& F, const bf16* PROJ, const bf16* ST, bf16* AO) { LTID();
;     ...
; #pragma unroll
;         for (int i = 0; i < 16; ++i) { float s1 = 0.f, s2 = 0.f;
; #pragma unroll
;             for (int eb = 0; eb < 8; ++eb) { s1 += o[eb][i]; s2 += o[eb][i] * o[eb][i]; }
;             s1 = half_sum32(s1); s2 = half_sum32(s2);
;             if (r32 == 0) { part[(e2 * 128 + rg * 32 + crow(i, hh)) * 2] = s1; part[(e2 * 128 + rg * 32 + crow(i, hh)) * 2 + 1] = s2; } }
	s_and_saveexec_b64 s[6:7], vcc
	s_add_i32 s0, 0, 0x20600
	v_lshl_add_u32 v134, v0, 3, s0
	v_pk_add_f32 v[130:131], v[132:133], v[130:131]
	ds_write_b64 v134, v[130:131] offset:192
	s_or_b64 exec, exec, s[6:7]
	v_add_f32_e32 v130, 0, v15
	v_mul_f32_e32 v131, v31, v31
	v_add_f32_e32 v130, v130, v31
	v_fmac_f32_e32 v131, v15, v15
	v_add_f32_e32 v130, v130, v47
	v_fmac_f32_e32 v131, v47, v47
	v_add_f32_e32 v130, v130, v63
	v_fmac_f32_e32 v131, v63, v63
	v_add_f32_e32 v130, v130, v79
	v_fmac_f32_e32 v131, v79, v79
	v_add_f32_e32 v130, v130, v95
	v_fmac_f32_e32 v131, v95, v95
	v_add_f32_e32 v130, v130, v111
	v_fmac_f32_e32 v131, v111, v111
	v_add_f32_e32 v130, v130, v127
	v_fmac_f32_e32 v131, v127, v127
	s_nop 0
	v_add_f32_dpp v130, v130, v130 quad_perm:[1,0,3,2] row_mask:0xf bank_mask:0xf bound_ctrl:1
	v_add_f32_dpp v131, v131, v131 quad_perm:[1,0,3,2] row_mask:0xf bank_mask:0xf bound_ctrl:1
	s_nop 0
	v_add_f32_dpp v130, v130, v130 quad_perm:[2,3,0,1] row_mask:0xf bank_mask:0xf bound_ctrl:1
	v_add_f32_dpp v131, v131, v131 quad_perm:[2,3,0,1] row_mask:0xf bank_mask:0xf bound_ctrl:1
	s_nop 0
	v_add_f32_dpp v130, v130, v130 row_half_mirror row_mask:0xf bank_mask:0xf bound_ctrl:1
	v_add_f32_dpp v131, v131, v131 row_half_mirror row_mask:0xf bank_mask:0xf bound_ctrl:1
	s_nop 0
	v_add_f32_dpp v130, v130, v130 row_mirror row_mask:0xf bank_mask:0xf bound_ctrl:1
	v_add_f32_dpp v131, v131, v131 row_mirror row_mask:0xf bank_mask:0xf bound_ctrl:1
	v_mov_b32_e32 v132, v130
	v_mov_b32_e32 v133, v131
	s_nop 1
	v_permlane16_swap_b32 v130, v132
	s_nop 1
	v_permlane16_swap_b32 v131, v133
	s_and_saveexec_b64 s[6:7], vcc
	s_add_i32 s0, 0, 0x20600
	v_lshl_add_u32 v134, v0, 3, s0
	v_pk_add_f32 v[130:131], v[132:133], v[130:131]
	ds_write_b64 v134, v[130:131] offset:200
	s_or_b64 exec, exec, s[6:7]
	v_add_f32_e32 v130, 0, v16
	v_mul_f32_e32 v131, v32, v32
	v_add_f32_e32 v130, v130, v32
	v_fmac_f32_e32 v131, v16, v16
	v_add_f32_e32 v130, v130, v48
	v_fmac_f32_e32 v131, v48, v48
	v_add_f32_e32 v130, v130, v64
	v_fmac_f32_e32 v131, v64, v64
	v_add_f32_e32 v130, v130, v80
	v_fmac_f32_e32 v131, v80, v80
	v_add_f32_e32 v130, v130, v96
	v_fmac_f32_e32 v131, v96, v96
	v_add_f32_e32 v130, v130, v112
	v_fmac_f32_e32 v131, v112, v112
	v_add_f32_e32 v130, v130, v128
	v_fmac_f32_e32 v131, v128, v128
	s_nop 0
	v_add_f32_dpp v130, v130, v130 quad_perm:[1,0,3,2] row_mask:0xf bank_mask:0xf bound_ctrl:1
	v_add_f32_dpp v131, v131, v131 quad_perm:[1,0,3,2] row_mask:0xf bank_mask:0xf bound_ctrl:1
	s_nop 0
	v_add_f32_dpp v130, v130, v130 quad_perm:[2,3,0,1] row_mask:0xf bank_mask:0xf bound_ctrl:1
	v_add_f32_dpp v131, v131, v131 quad_perm:[2,3,0,1] row_mask:0xf bank_mask:0xf bound_ctrl:1
	s_nop 0
	v_add_f32_dpp v130, v130, v130 row_half_mirror row_mask:0xf bank_mask:0xf bound_ctrl:1
	v_add_f32_dpp v131, v131, v131 row_half_mirror row_mask:0xf bank_mask:0xf bound_ctrl:1
	s_nop 0
	v_add_f32_dpp v130, v130, v130 row_mirror row_mask:0xf bank_mask:0xf bound_ctrl:1
	v_add_f32_dpp v131, v131, v131 row_mirror row_mask:0xf bank_mask:0xf bound_ctrl:1
	v_mov_b32_e32 v132, v130
	v_mov_b32_e32 v133, v131
	s_nop 1
	v_permlane16_swap_b32 v130, v132
	s_nop 1
	v_permlane16_swap_b32 v131, v133
	s_and_saveexec_b64 s[6:7], vcc
	s_add_i32 s0, 0, 0x20600
	v_lshl_add_u32 v134, v0, 3, s0
	v_pk_add_f32 v[130:131], v[132:133], v[130:131]
	ds_write_b64 v134, v[130:131] offset:208
	s_or_b64 exec, exec, s[6:7]
	v_add_f32_e32 v130, 0, v17
	v_mul_f32_e32 v131, v33, v33
	v_add_f32_e32 v130, v130, v33
	v_fmac_f32_e32 v131, v17, v17
	v_add_f32_e32 v130, v130, v49
	v_fmac_f32_e32 v131, v49, v49
	v_add_f32_e32 v130, v130, v65
	v_fmac_f32_e32 v131, v65, v65
	v_add_f32_e32 v130, v130, v81
	v_fmac_f32_e32 v131, v81, v81
	v_add_f32_e32 v130, v130, v97
	v_fmac_f32_e32 v131, v97, v97
	v_add_f32_e32 v130, v130, v113
	v_fmac_f32_e32 v131, v113, v113
	v_add_f32_e32 v130, v130, v129
	v_fmac_f32_e32 v131, v129, v129
	s_nop 0
	v_add_f32_dpp v130, v130, v130 quad_perm:[1,0,3,2] row_mask:0xf bank_mask:0xf bound_ctrl:1
	v_add_f32_dpp v131, v131, v131 quad_perm:[1,0,3,2] row_mask:0xf bank_mask:0xf bound_ctrl:1
	s_nop 0
	v_add_f32_dpp v130, v130, v130 quad_perm:[2,3,0,1] row_mask:0xf bank_mask:0xf bound_ctrl:1
	v_add_f32_dpp v131, v131, v131 quad_perm:[2,3,0,1] row_mask:0xf bank_mask:0xf bound_ctrl:1
	s_nop 0
	v_add_f32_dpp v130, v130, v130 row_half_mirror row_mask:0xf bank_mask:0xf bound_ctrl:1
	v_add_f32_dpp v131, v131, v131 row_half_mirror row_mask:0xf bank_mask:0xf bound_ctrl:1
	s_nop 0
	v_add_f32_dpp v130, v130, v130 row_mirror row_mask:0xf bank_mask:0xf bound_ctrl:1
	v_add_f32_dpp v131, v131, v131 row_mirror row_mask:0xf bank_mask:0xf bound_ctrl:1
	v_mov_b32_e32 v132, v130
	v_mov_b32_e32 v133, v131
	s_nop 1
	v_permlane16_swap_b32 v130, v132
	s_nop 1
	v_permlane16_swap_b32 v131, v133
	s_and_saveexec_b64 s[6:7], vcc
	s_cbranch_execz .LBB0_364
	s_add_i32 s0, 0, 0x20600
	v_lshl_add_u32 v0, v0, 3, s0
	v_pk_add_f32 v[130:131], v[132:133], v[130:131]
	ds_write_b64 v0, v[130:131] offset:216
	s_branch .LBB0_364

; __device__ __forceinline__ float half_max32(float v) { v = row_max16(v); float a; const float b = swap16_other(v, a); return __builtin_fmaxf(a, b); }
; __device__ __forceinline__ float xor32_sum(float v) { float a; const float b = swap32_other(v, a); return a + b; }
; #define GAS __attribute__((address_space(1)))
; #define LDS_WAIT() asm volatile("s_waitcnt lgkmcnt(0)" ::: "memory")
; __device__ __forceinline__ void da_attn_phase(Frame& F, const bf16* QKV, bf16* AO, float lam, float one_m_li, const float* subg, const unsigned* kmax, gu32* qctr, const ConvJob& cj) { LTID();
;     ...
;         const int h = 7 - (U >> 8), qb = 63 - ((U & 255) >> 2), b = U & 3;
;         const int q0 = qb * 128, NT = 2 * qb + 2;
;         const float sl2 = __builtin_amdgcn_exp2f(-(float)(h + 1)) * LOG2E;
;         const size_t rowbase = (size_t)b * SEQ;
;         const unsigned* kmp = kmax + ((b * 16 + h * 2 + mp) * 2);
;         const float km2 = __builtin_bit_cast(float, __hip_atomic_load(kmp, RLX_AGENT)) + __builtin_bit_cast(float, __hip_atomic_load(kmp + 1, RLX_AGENT));
;         bf16x8 qr[4];
;         { const bf16* qp = QKV + (rowbase + q0 + rg * 32 + r32) * 3072 + h * 128 + mp * 64 + hh * 8;
; #pragma unroll
;           for (int d0 = 0; d0 < 4; ++d0) qr[d0] = *(const GAS bf16x8*)(qp + d0 * 16); }
;         int t_min = 0; float qkw = 0.f;
;         { float qs = 0.f;
; #pragma unroll
;           for (int d0 = 0; d0 < 4; ++d0)
; #pragma unroll
;               for (int j = 0; j < 8; ++j) { const float qv = bf2f((unsigned short)qr[d0][j]); qs += qv * qv; }
;           qs = xor32_sum(qs); qs = half_max32(qs);
;           const float bw = 2.0f * sqrtf(qs * km2) * 1.02f;
;           qkw = 0.5f * bw;
;           if (lane == 0) wred[wid] = bw;
;           LDS_WAIT(); __syncthreads();
.LBB0_674:
	s_or_b64 exec, exec, s[6:7]
	s_ashr_i32 s24, s2, 8
	s_sub_i32 s8, 7, s24
	s_not_b32 s0, s2
	s_and_b32 s2, s2, 3
	s_ashr_i32 s28, s22, 6
	s_lshl_b32 s23, s2, 13
	s_lshl_b32 s2, s2, 4
	s_lshl_b32 s6, s8, 1
	s_and_b32 s61, s28, 1
	s_add_i32 s6, s6, s2
	s_or_b32 s2, s61, s6
	s_bfe_u32 s0, s0, 0x60002
	s_lshl_b32 s78, s2, 1
	s_ashr_i32 s64, s22, 7
	s_lshl_b32 s29, s0, 7
	s_lshl_b64 s[6:7], s[78:79], 2
	s_add_u32 s6, s38, s6
	s_addc_u32 s7, s39, s7
	s_lshl_b32 s60, s64, 5
	s_or_b32 s20, s29, s23
	s_ashr_i32 s2, s60, 31
	v_and_b32_e32 v241, 31, v238
	global_load_dword v4, v1, s[6:7] sc1
	global_load_dword v5, v1, s[6:7] offset:4 sc1
	s_add_u32 s6, s60, s20
	v_or_b32_e32 v0, s6, v241
	v_mov_b64_e32 v[2:3], s[14:15]
	s_movk_i32 s6, 0x1800
	s_addc_u32 s2, s2, 0
	v_mad_u64_u32 v[2:3], s[6:7], v0, s6, v[2:3]
	v_mov_b32_e32 v0, 0x1800
	v_mad_i32_i24 v3, s2, v0, v3
	s_lshl_b32 s78, s8, 8
	v_bfe_u32 v243, v238, 5, 1
	v_lshl_add_u64 v[2:3], v[2:3], 0, s[78:79]
	s_lshl_b32 s78, s61, 7
	v_lshl_add_u64 v[2:3], v[2:3], 0, s[78:79]
	v_lshlrev_b32_e32 v0, 4, v243
	v_lshl_add_u64 v[2:3], v[2:3], 0, v[0:1]
	global_load_dwordx4 v[164:167], v[2:3], off
	global_load_dwordx4 v[168:171], v[2:3], off offset:32
	global_load_dwordx4 v[172:175], v[2:3], off offset:64
	global_load_dwordx4 v[176:179], v[2:3], off offset:96
	v_and_b32_e32 v244, 63, v238
	s_mov_b32 s21, s79
	s_lshl_b32 s30, s8, 7
	s_waitcnt vmcnt(3)
	v_and_b32_e32 v0, 0xffff0000, v164
	v_lshlrev_b32_e32 v2, 16, v164
	v_mul_f32_e32 v0, v0, v0
	v_fmac_f32_e32 v0, v2, v2
	v_lshlrev_b32_e32 v2, 16, v165
	v_fmac_f32_e32 v0, v2, v2
	v_and_b32_e32 v2, 0xffff0000, v165
	v_fmac_f32_e32 v0, v2, v2
	v_lshlrev_b32_e32 v2, 16, v166
	v_fmac_f32_e32 v0, v2, v2
	v_and_b32_e32 v2, 0xffff0000, v166
	v_fmac_f32_e32 v0, v2, v2
	v_lshlrev_b32_e32 v2, 16, v167
	v_fmac_f32_e32 v0, v2, v2
	v_and_b32_e32 v2, 0xffff0000, v167
	v_fmac_f32_e32 v0, v2, v2
	s_waitcnt vmcnt(2)
	v_lshlrev_b32_e32 v2, 16, v168
	v_fmac_f32_e32 v0, v2, v2
	v_and_b32_e32 v2, 0xffff0000, v168
	v_fmac_f32_e32 v0, v2, v2
	v_lshlrev_b32_e32 v2, 16, v169
	v_fmac_f32_e32 v0, v2, v2
	v_and_b32_e32 v2, 0xffff0000, v169
	v_fmac_f32_e32 v0, v2, v2
	v_lshlrev_b32_e32 v2, 16, v170
	v_fmac_f32_e32 v0, v2, v2
	v_and_b32_e32 v2, 0xffff0000, v170
	v_fmac_f32_e32 v0, v2, v2
	v_lshlrev_b32_e32 v2, 16, v171
	v_fmac_f32_e32 v0, v2, v2
	v_and_b32_e32 v2, 0xffff0000, v171
	v_fmac_f32_e32 v0, v2, v2
	s_waitcnt vmcnt(1)
	v_lshlrev_b32_e32 v2, 16, v172
	v_fmac_f32_e32 v0, v2, v2
	v_and_b32_e32 v2, 0xffff0000, v172
	v_fmac_f32_e32 v0, v2, v2
	v_lshlrev_b32_e32 v2, 16, v173
	v_fmac_f32_e32 v0, v2, v2
	v_and_b32_e32 v2, 0xffff0000, v173
	v_fmac_f32_e32 v0, v2, v2
	v_lshlrev_b32_e32 v2, 16, v174
	v_fmac_f32_e32 v0, v2, v2
	v_and_b32_e32 v2, 0xffff0000, v174
	v_fmac_f32_e32 v0, v2, v2
	v_lshlrev_b32_e32 v2, 16, v175
	v_fmac_f32_e32 v0, v2, v2
	v_and_b32_e32 v2, 0xffff0000, v175
	v_fmac_f32_e32 v0, v2, v2
	s_waitcnt vmcnt(0)
	v_lshlrev_b32_e32 v2, 16, v176
	v_fmac_f32_e32 v0, v2, v2
	v_and_b32_e32 v2, 0xffff0000, v176
	v_fmac_f32_e32 v0, v2, v2
	v_lshlrev_b32_e32 v2, 16, v177
	v_fmac_f32_e32 v0, v2, v2
	v_and_b32_e32 v2, 0xffff0000, v177
	v_fmac_f32_e32 v0, v2, v2
	v_lshlrev_b32_e32 v2, 16, v178
	v_fmac_f32_e32 v0, v2, v2
	v_and_b32_e32 v2, 0xffff0000, v178
	v_fmac_f32_e32 v0, v2, v2
	v_lshlrev_b32_e32 v2, 16, v179
	v_fmac_f32_e32 v0, v2, v2
	v_and_b32_e32 v2, 0xffff0000, v179
	v_fmac_f32_e32 v0, v2, v2
	v_mov_b32_e32 v3, v0
	s_nop 1
	v_permlane32_swap_b32 v3, v0
	v_add_f32_e32 v2, v4, v5
	v_add_f32_e32 v0, v0, v3
	s_nop 1
	v_mov_b32_dpp v3, v0 quad_perm:[1,0,3,2] row_mask:0xf bank_mask:0xf bound_ctrl:1
	v_max_f32_e32 v3, v3, v3
	v_max_f32_e32 v0, v0, v3
	s_nop 1
	v_mov_b32_dpp v3, v0 quad_perm:[2,3,0,1] row_mask:0xf bank_mask:0xf bound_ctrl:1
	v_max_f32_e32 v3, v3, v3
	v_max_f32_e32 v0, v0, v3
	s_nop 1
	v_mov_b32_dpp v3, v0 row_half_mirror row_mask:0xf bank_mask:0xf bound_ctrl:1
	v_max_f32_e32 v3, v3, v3
	v_max_f32_e32 v0, v0, v3
	s_nop 1
	v_mov_b32_dpp v3, v0 row_mirror row_mask:0xf bank_mask:0xf bound_ctrl:1
	v_max_f32_e32 v3, v3, v3
	v_max_f32_e32 v0, v0, v3
	v_mov_b32_e32 v3, v0
	s_nop 1
	v_permlane16_swap_b32 v3, v0
	s_nop 0
	v_max_f32_e32 v3, v3, v3
	v_max_f32_e32 v0, v0, v0
	v_max_f32_e32 v0, v0, v3
	v_mul_f32_e32 v0, v2, v0
	v_cmp_gt_f32_e32 vcc, s3, v0
	v_mul_f32_e32 v2, 0x4f800000, v0
	s_nop 0
	v_cndmask_b32_e32 v0, v0, v2, vcc
	v_sqrt_f32_e32 v2, v0
	s_nop 0
	v_add_u32_e32 v3, -1, v2
	v_fma_f32 v4, -v3, v2, v0
	v_cmp_ge_f32_e64 s[6:7], 0, v4
	v_add_u32_e32 v4, 1, v2
	s_nop 0
	v_cndmask_b32_e64 v3, v2, v3, s[6:7]
	v_fma_f32 v2, -v4, v2, v0
	v_cmp_lt_f32_e64 s[6:7], 0, v2
	s_nop 1
	v_cndmask_b32_e64 v2, v3, v4, s[6:7]
	v_mul_f32_e32 v3, 0x37800000, v2
	v_cndmask_b32_e32 v2, v2, v3, vcc
	v_cmp_class_f32_e32 vcc, v0, v229
	v_cmp_eq_u32_e64 s[6:7], 0, v244
	s_nop 0
	v_cndmask_b32_e32 v0, v2, v0, vcc
	v_add_f32_e32 v0, v0, v0
	v_mul_f32_e32 v36, 0x3f828f5c, v0
	s_and_saveexec_b64 s[8:9], s[6:7]
	s_lshl_b32 s2, s28, 2
	s_add_i32 s2, s2, 0
	s_add_i32 s2, s2, 0x21040
	v_mov_b32_e32 v0, s2
	ds_write_b32 v0, v36
	s_or_b64 exec, exec, s[8:9]
	s_sub_i32 s2, 8, s24
	v_cvt_f32_u32_e32 v0, s2
	s_add_i32 s2, 0, 0x21040
	v_mov_b32_e32 v2, s2
	s_waitcnt lgkmcnt(0)
	v_exp_f32_e64 v0, -v0
	s_waitcnt lgkmcnt(0)
	s_barrier
; #define DMA_K(it_, ks) do { const size_t to_ = (size_t)(NT - 1 - (it_)) * 64 * 3072; const unsigned sb_ = (unsigned)(ks) * 16384u; \
;         glds16(kg0 + to_, (unsigned)__builtin_amdgcn_readfirstlane(kd0 + sb_)); glds16(kg0 + to_ + 64, (unsigned)__builtin_amdgcn_readfirstlane(kd0 + sb_ + 8192)); } while (0)
; #define DMA_V(it_, vs) do { const size_t to_ = (size_t)(NT - 1 - (it_)) * 64 * 3072; const unsigned sb_ = (unsigned)(vs) * 16384u; \
;         glds16(vg0 + to_, (unsigned)__builtin_amdgcn_readfirstlane(vd0 + sb_)); glds16(vg0 + to_ + 64, (unsigned)__builtin_amdgcn_readfirstlane(vd0 + sb_ + 8192)); } while (0)
; __device__ __forceinline__ void da_attn_phase(Frame& F, const bf16* QKV, bf16* AO, float lam, float one_m_li, const float* subg, const unsigned* kmax, gu32* qctr, const ConvJob& cj) { LTID();
;     ...
;           float bm = wred[0];
; #pragma unroll
;           for (int w8 = 1; w8 < 8; ++w8) bm = __builtin_fmaxf(bm, wred[w8]);
;           const float Wk = (bm + 38.0f) / sl2, xx = ((float)q0 - Wk - 63.0f) * (1.0f / 64.0f);
;           t_min = (xx > 0.f) ? (int)ceilf(xx) : 0; t_min = __builtin_amdgcn_readfirstlane(t_min); }
;         int NIT = NT - t_min;
;         const bf16* kg0 = QKV + (rowbase + lane) * 3072 + 1024 + h * 128 + wid * 8;
;         const bf16* vg0 = QKV + (rowbase + 16 * (wid & 3) + (lane >> 2)) * 3072 + 2048 + h * 128 + (wid >> 2) * 32 + (lane & 3) * 8;
;         const unsigned ldsb = (unsigned)(uintptr_t)lds, kd0 = ldsb + wid * 1024, vd0 = ldsb + 49152 + (wid >> 2) * 4096 + (wid & 3) * 1024;
;     ...
;         float tmax = -INFINITY;
;         float m_ref = -qkw, l_run = 0.f; f32x16 o[4];
; #pragma unroll
;         for (int eb = 0; eb < 4; ++eb) o[eb] = (f32x16){0.f, 0.f, 0.f, 0.f, 0.f, 0.f, 0.f, 0.f, 0.f, 0.f, 0.f, 0.f, 0.f, 0.f, 0.f, 0.f};
;         const float hb = sl2 * (float)(4 * hh);
;         DMA_K(0, 0); DMA_K(1, 1); DMA_V(0, 0);
;         if (NIT > 2) { DMA_K(2, 2); DMA_V(1, 1); asm volatile("s_waitcnt vmcnt(8)\n\ts_barrier" ::: "memory"); }
;         else { DMA_V(1, 1); asm volatile("s_waitcnt vmcnt(6)\n\ts_barrier" ::: "memory"); }
	ds_read_b128 v[2:5], v2
	v_readlane_b32 s2, v254, 9
	v_mul_f32_e32 v188, 0x3fb8aa3b, v0
	v_cvt_f32_u32_e32 v99, s29
	v_mov_b32_e32 v0, s2
	ds_read_b128 v[6:9], v0
	s_waitcnt lgkmcnt(1)
	v_max_f32_e32 v0, v3, v3
	v_max_f32_e32 v2, v2, v2
	v_max_f32_e32 v0, v2, v0
	v_max3_f32 v0, v0, v4, v5
	s_waitcnt lgkmcnt(0)
	v_max3_f32 v0, v0, v6, v7
	v_max3_f32 v0, v0, v8, v9
	v_add_f32_e32 v0, 0x42180000, v0
	v_div_scale_f32 v2, s[8:9], v188, v188, v0
	v_rcp_f32_e32 v3, v2
	s_bfe_u32 s9, s22, 0x20006
	s_ashr_i32 s22, s22, 8
	s_lshl_b32 s26, s22, 5
	v_fma_f32 v4, -v2, v3, 1.0
	v_fmac_f32_e32 v3, v4, v3
	v_div_scale_f32 v4, vcc, v0, v188, v0
	v_mul_f32_e32 v5, v4, v3
	v_fma_f32 v6, -v2, v5, v4
	v_fmac_f32_e32 v5, v6, v3
	v_fma_f32 v2, -v2, v5, v4
	v_div_fmas_f32 v2, v2, v3, v5
	v_div_fixup_f32 v0, v2, v188, v0
	v_sub_f32_e32 v0, v99, v0
	v_add_f32_e32 v0, 0xc27c0000, v0
	v_mul_f32_e32 v0, 0x3c800000, v0
	v_ceil_f32_e32 v2, v0
	v_cvt_i32_f32_e32 v2, v2
	v_cmp_lt_f32_e32 vcc, 0, v0
	v_lshrrev_b32_e32 v4, 2, v244
	v_lshl_or_b32 v4, s9, 4, v4
	v_cndmask_b32_e32 v0, 0, v2, vcc
	v_or_b32_e32 v4, s23, v4
	v_readfirstlane_b32 s8, v0
	v_or_b32_e32 v0, s23, v244
	v_mul_u32_u24_e32 v0, 0xc00, v0
	s_lshl_b32 s22, s22, 12
	v_lshlrev_b32_e32 v0, 1, v0
	v_mul_u32_u24_e32 v4, 0xc00, v4
	s_add_i32 s22, s22, 0
	s_lshl_b32 s9, s9, 10
	v_lshl_add_u64 v[2:3], s[14:15], 0, v[0:1]
	s_lshl_b32 s24, s28, 3
	v_lshlrev_b32_e32 v34, 1, v4
	v_mov_b32_e32 v35, v1
	s_add_i32 s69, s22, s9
	s_lshl_b32 s22, s30, 1
	s_mov_b32 s23, s79
	v_lshlrev_b32_e32 v124, 3, v238
	s_ashr_i32 s25, s24, 31
	v_lshl_add_u64 v[4:5], s[14:15], 0, v[34:35]
	v_lshl_add_u64 v[2:3], v[2:3], 0, s[22:23]
	s_lshl_b32 s2, s0, 1
	v_and_b32_e32 v37, 24, v124
	s_ashr_i32 s27, s26, 31
	v_lshl_add_u64 v[186:187], s[24:25], 1, v[2:3]
	v_lshl_add_u64 v[2:3], v[4:5], 0, s[22:23]
	s_add_i32 s68, s2, 2
	v_lshl_add_u64 v[2:3], s[26:27], 1, v[2:3]
	v_lshlrev_b32_e32 v4, 1, v37
	v_mov_b32_e32 v5, v1
	s_sub_i32 s70, s68, s8
	v_lshl_add_u64 v[2:3], v[2:3], 0, v[4:5]
	s_mov_b64 s[8:9], 0x1000
	s_or_b32 s71, s2, 1
	v_lshl_add_u64 v[184:185], v[2:3], 0, s[8:9]
	s_mul_i32 s8, s71, 0x60000
	s_mov_b32 s9, s79
	s_lshl_b32 s72, s28, 10
	v_lshl_add_u64 v[2:3], v[186:187], 0, s[8:9]
	s_mov_b64 s[12:13], 0x800
	s_add_i32 s72, s72, 0
	v_lshl_add_u64 v[4:5], v[2:3], 0, s[12:13]
	s_mov_b32 m0, s72
	s_nop 0
	global_load_lds_dwordx4 v[4:5], off
	s_mov_b64 s[34:35], 0x880
	s_add_i32 s23, s72, 0x2000
	v_lshl_add_u64 v[2:3], v[2:3], 0, s[34:35]
	s_mov_b32 m0, s23
	s_nop 0
	global_load_lds_dwordx4 v[2:3], off
	s_mul_i32 s23, s0, 0x60000
	s_lshl_b32 s78, s23, 1
	v_lshl_add_u64 v[4:5], v[186:187], 0, s[78:79]
	v_lshl_add_u64 v[2:3], v[4:5], 0, s[12:13]
	s_add_i32 s23, s72, 0x4000
	s_mov_b32 m0, s23
	s_nop 0
	global_load_lds_dwordx4 v[2:3], off
	v_lshl_add_u64 v[4:5], v[4:5], 0, s[34:35]
	s_add_i32 s23, s72, 0x6000
	s_mov_b32 m0, s23
	s_nop 0
	global_load_lds_dwordx4 v[4:5], off
	s_add_i32 s69, s69, 0xc000
	v_lshl_add_u64 v[4:5], v[184:185], 0, s[8:9]
	s_mov_b32 m0, s69
	s_nop 0
	global_load_lds_dwordx4 v[4:5], off
	v_lshl_add_u64 v[4:5], v[4:5], 0, s[54:55]
	s_add_i32 s8, s69, 0x2000
	s_mov_b32 m0, s8
	s_nop 0
	global_load_lds_dwordx4 v[4:5], off
	s_mov_b64 s[10:11], 0x880
	s_cmp_lt_i32 s70, 3
	s_mov_b64 s[8:9], -1
	s_cbranch_scc0 .LBB0_678
	v_lshl_add_u64 v[4:5], v[184:185], 0, s[78:79]
	s_add_i32 s8, s69, 0x4000
	s_mov_b32 m0, s8
	s_nop 0
	global_load_lds_dwordx4 v[4:5], off
	v_lshl_add_u64 v[4:5], v[4:5], 0, s[54:55]
	s_add_i32 s8, s69, 0x6000
	s_mov_b32 m0, s8
	s_nop 0
	global_load_lds_dwordx4 v[4:5], off
	s_waitcnt vmcnt(6)
	s_barrier
	s_mov_b64 s[8:9], 0
.LBB0_678:
	v_mov_b32_e32 v189, 0x20000
	s_andn2_b64 vcc, exec, s[8:9]
	s_cbranch_vccnz .LBB0_680
	s_mov_b32 s8, 0xfffa0000
	s_mov_b32 s9, -1
	v_lshl_add_u64 v[4:5], v[2:3], 0, s[8:9]
	s_add_i32 s8, s72, 0x8000
	s_mov_b32 m0, s8
	s_nop 0
	global_load_lds_dwordx4 v[4:5], off
	s_mov_b32 s8, 0xfffa0080
	s_mov_b32 s9, -1
	v_lshl_add_u64 v[2:3], v[2:3], 0, s[8:9]
	s_add_i32 s8, s72, 0xa000
	s_mov_b32 m0, s8
	s_nop 0
	global_load_lds_dwordx4 v[2:3], off
	v_lshl_add_u64 v[2:3], v[184:185], 0, s[78:79]
	s_add_i32 s8, s69, 0x4000
	s_mov_b32 m0, s8
	s_nop 0
	global_load_lds_dwordx4 v[2:3], off
	v_lshl_add_u64 v[2:3], v[2:3], 0, s[54:55]
	s_add_i32 s8, s69, 0x6000
	s_mov_b32 m0, s8
	s_nop 0
	global_load_lds_dwordx4 v[2:3], off
	s_waitcnt vmcnt(8)
	s_barrier

.LBB0_688:
	s_add_i32 s46, s44, -1
	s_cmp_lt_i32 s46, s70
	s_cselect_b64 s[26:27], -1, 0
	s_cmp_ge_i32 s46, s70
	s_cselect_b64 s[28:29], -1, 0
	s_and_b64 vcc, exec, s[28:29]
	s_cbranch_vccnz .LBB0_690
	s_lshl_b32 s2, s65, 14
	v_lshl_add_u64 v[132:133], v[224:225], 0, s[22:23]
	s_add_i32 s2, s2, s72
	s_mov_b32 m0, s2
	s_nop 0
	global_load_lds_dwordx4 v[132:133], off
	v_lshl_add_u64 v[132:133], v[132:133], 0, s[54:55]
	s_addk_i32 s2, 0x2000
	s_mov_b32 m0, s2
	s_nop 0
	global_load_lds_dwordx4 v[132:133], off
.LBB0_690:
	s_cmp_lt_i32 s0, s70
	s_cselect_b64 s[24:25], -1, 0
	s_cmp_ge_i32 s0, s70
	s_cselect_b64 s[30:31], -1, 0
	s_and_b64 vcc, exec, s[30:31]
	v_lshl_add_u64 v[226:227], v[222:223], 0, s[22:23]
	s_cbranch_vccnz .LBB0_692
	s_lshl_b32 s2, s65, 14
	s_addk_i32 s2, 0xc000
	s_cmp_lg_u32 s65, 0
	s_cselect_b32 s2, s2, 0x8000
	s_mov_b64 s[34:35], 0x3ffa1000
	v_lshl_add_u64 v[132:133], v[226:227], 0, s[34:35]
	s_add_i32 s2, s2, s69
	s_mov_b32 m0, s2
	s_nop 0
	global_load_lds_dwordx4 v[132:133], off
	s_mov_b64 s[34:35], 0x3ffa1080
	v_lshl_add_u64 v[132:133], v[226:227], 0, s[34:35]
	s_addk_i32 s2, 0x2000
	s_mov_b32 m0, s2
	s_nop 0
	global_load_lds_dwordx4 v[132:133], off

.LBB0_707:
	v_mov_b32_e32 v0, 0x60000
	s_lshl_b32 s2, s47, 14
	v_mad_i64_i32 v[66:67], s[28:29], s43, v0, v[186:187]
	s_mov_b64 s[12:13], 0x800
	v_lshl_add_u64 v[68:69], v[66:67], 0, s[12:13]
	s_add_i32 s2, s2, s72
	s_mov_b32 m0, s2
	s_nop 0
	global_load_lds_dwordx4 v[68:69], off
	v_lshl_add_u64 v[66:67], v[66:67], 0, s[10:11]
	s_addk_i32 s2, 0x2000
	s_mov_b32 m0, s2
	s_nop 0
	global_load_lds_dwordx4 v[66:67], off
	s_andn2_b64 vcc, exec, s[26:27]
	s_cbranch_vccz .LBB0_711
	s_branch .LBB0_712

.LBB0_711:
	s_lshl_b32 s2, s47, 14
	s_addk_i32 s2, 0xc000
	s_cmp_lg_u32 s47, 0
	s_cselect_b32 s2, s2, 0x8000
	s_mov_b64 s[26:27], 0x3ff41000
	v_lshl_add_u64 v[66:67], v[226:227], 0, s[26:27]
	s_add_i32 s2, s2, s69
	s_mov_b32 m0, s2
	s_nop 0
	global_load_lds_dwordx4 v[66:67], off
	s_mov_b64 s[26:27], 0x3ff41080
	v_lshl_add_u64 v[66:67], v[226:227], 0, s[26:27]
	s_addk_i32 s2, 0x2000
	s_mov_b32 m0, s2
	s_nop 0
	global_load_lds_dwordx4 v[66:67], off

.LBB0_734:
	s_sub_i32 s0, s71, s2
	s_lshl_b32 s2, s65, 14
	s_addk_i32 s2, 0xc000
	s_cmp_lg_u32 s65, 0
	s_cselect_b32 s2, s2, 0x8000
	v_mov_b32_e32 v0, 0x60000
	v_mad_i64_i32 v[100:101], s[6:7], s0, v0, v[184:185]
	s_add_i32 s0, s2, s69
	s_mov_b32 m0, s0
	s_nop 0
	global_load_lds_dwordx4 v[100:101], off
	v_lshl_add_u64 v[100:101], v[100:101], 0, s[54:55]
	s_addk_i32 s0, 0x2000
	s_mov_b32 m0, s0
	s_nop 0
	global_load_lds_dwordx4 v[100:101], off

.LBB0_749:
	s_sub_i32 s0, s71, s0
	v_mov_b32_e32 v0, 0x60000
	v_mad_i64_i32 v[100:101], s[6:7], s0, v0, v[186:187]
	s_lshl_b32 s8, s65, 14
	s_mov_b64 s[6:7], 0x800
	v_lshl_add_u64 v[102:103], v[100:101], 0, s[6:7]
	s_add_i32 s0, s8, s72
	s_mov_b32 m0, s0
	s_nop 0
	global_load_lds_dwordx4 v[102:103], off
	v_lshl_add_u64 v[100:101], v[100:101], 0, s[10:11]
	s_addk_i32 s0, 0x2000
	s_mov_b32 m0, s0
	s_nop 0
	global_load_lds_dwordx4 v[100:101], off
	s_cmp_ge_i32 s2, s70
	s_cbranch_scc0 .LBB0_734
	s_branch .LBB0_735
